# speedup vs baseline: 1.0044x; 1.0044x over previous
_Z9proj_gemmPKfS0_S0_PK14__hip_bfloat16S0_S0_S0_PS1_:
	s_lshl_b32 s3, s2, 2
	s_load_dwordx8 s[8:15], s[0:1], 0x0
	s_and_b32 s3, s3, 28
	s_bfe_u32 s30, s2, 0x20005
	s_lshr_b32 s6, s2, 3
	s_ashr_i32 s18, s2, 7
	s_lshr_b32 s7, s2, 5
	s_or_b32 s20, s3, s30
	s_bfe_u32 s3, s2, 0x20003
	s_cmpk_lt_u32 s2, 0x80
	s_cselect_b64 s[16:17], -1, 0
	s_and_b64 s[4:5], s[16:17], exec
	s_waitcnt lgkmcnt(0)
	s_cselect_b32 s4, s9, s11
	s_cselect_b32 s5, s8, s10
	s_lshl_b32 s24, s20, 18
	s_lshl_b32 s8, s20, 20
	s_add_u32 s25, s5, s8
	s_addc_u32 s26, s4, 0
	s_ashr_i32 s19, s18, 31
	s_lshl_b64 s[4:5], s[18:19], 21
	s_add_u32 s4, s14, s4
	s_addc_u32 s5, s15, s5
	s_lshl_b32 s8, s3, 19
	s_add_u32 s27, s4, s8
	s_addc_u32 s28, s5, 0
	s_xor_b32 s6, s6, s18
	v_lshlrev_b32_e32 v1, 4, v0
	s_lshl_b32 s34, s6, 4
	v_lshlrev_b32_e32 v2, 3, v0
	v_and_b32_e32 v3, 0x1f0, v1
	s_movk_i32 s6, 0x200
	s_lshl_b32 s4, s20, 1
	s_mul_i32 s31, s18, 5
	s_xor_b32 s7, s7, s18
	v_lshrrev_b32_e32 v28, 6, v0
	s_and_b32 s35, s34, 16
	v_and_or_b32 v29, v2, s6, v3
	v_lshrrev_b32_e32 v2, 1, v0
	v_and_b32_e32 v3, 48, v1
	s_add_i32 s4, s4, s31
	v_bitop3_b32 v2, v2, v3, 32 bitop3:0x6c
	v_or_b32_e32 v30, s35, v28
	s_lshl_b32 s38, s7, 4
	s_and_b32 s5, s4, 15
	v_lshrrev_b32_e32 v2, 1, v2
	v_or_b32_e32 v32, 8, v30
	s_and_b32 s39, s38, 16
	v_and_or_b32 v178, v0, 32, v2
	v_lshlrev_b32_e32 v2, 3, v30
	v_lshrrev_b32_e32 v31, 6, v29
	s_movk_i32 s36, 0xb0
	v_lshlrev_b32_e32 v3, 3, v32
	s_movk_i32 s37, 0xf0
	v_or_b32_e32 v33, s39, v28
	s_lshl_b32 s33, s4, 6
	s_lshl_b32 s4, s5, 8
	v_and_or_b32 v2, v2, s36, v31
	v_and_or_b32 v12, v3, s37, v31
	v_lshlrev_b32_e32 v3, 3, v33
	v_or_b32_e32 v34, 8, v33
	s_add_u32 s20, s25, s4
	v_mov_b32_e32 v183, 0
	v_and_or_b32 v20, v3, s36, v31
	v_lshlrev_b32_e32 v3, 3, v34
	s_addc_u32 s21, s26, 0
	v_lshlrev_b32_e32 v180, 12, v2
	v_mov_b32_e32 v181, v183
	v_and_or_b32 v22, v3, s37, v31
	v_lshl_add_u64 v[2:3], s[20:21], 0, v[180:181]
	v_lshlrev_b32_e32 v182, 2, v178
	v_lshl_add_u64 v[10:11], v[2:3], 0, v[182:183]
	v_lshlrev_b32_e32 v184, 12, v12
	v_mov_b32_e32 v185, v183
	s_lshl_b32 s4, s5, 7
	global_load_dwordx4 v[2:5], v[10:11], off offset:16
	global_load_dwordx4 v[6:9], v[10:11], off
	v_lshl_add_u64 v[10:11], s[20:21], 0, v[184:185]
	s_add_u32 s22, s27, s4
	v_lshl_add_u64 v[14:15], v[10:11], 0, v[182:183]
	s_addc_u32 s23, s28, 0
	v_lshlrev_b32_e32 v186, 11, v20
	v_mov_b32_e32 v187, v183
	global_load_dwordx4 v[10:13], v[14:15], off offset:16
	global_load_dwordx4 v[16:19], v[14:15], off
	v_lshl_add_u64 v[20:21], s[22:23], 0, v[186:187]
	v_lshlrev_b32_e32 v14, 1, v178
	v_mov_b32_e32 v15, v183
	v_lshlrev_b32_e32 v188, 11, v22
	v_mov_b32_e32 v189, v183
	v_lshl_add_u64 v[24:25], v[20:21], 0, v[14:15]
	v_lshl_add_u64 v[20:21], s[22:23], 0, v[188:189]
	v_lshl_add_u64 v[26:27], v[20:21], 0, v[14:15]
	global_load_dwordx4 v[20:23], v[24:25], off
	global_load_dwordx4 v[50:53], v[26:27], off
	v_bfe_u32 v24, v0, 5, 1
	v_and_or_b32 v25, v30, 22, v24
	v_lshl_or_b32 v208, v25, 10, v29
	v_and_or_b32 v25, v32, 30, v24
	v_lshl_or_b32 v205, v25, 10, v29
	v_bitop3_b32 v25, s34, 16, v28 bitop3:0x26
	v_and_or_b32 v26, v25, 22, v24
	v_lshl_or_b32 v204, v26, 10, v29
	v_bitop3_b32 v26, s35, v28, 24 bitop3:0xde
	v_and_or_b32 v27, v26, 30, v24
	v_lshl_or_b32 v201, v27, 10, v29
	v_and_or_b32 v27, v33, 22, v24
	v_lshl_or_b32 v206, v27, 10, v29
	v_and_or_b32 v27, v34, 30, v24
	s_load_dwordx8 s[4:11], s[0:1], 0x20
	v_lshl_or_b32 v207, v27, 10, v29
	v_bitop3_b32 v27, s38, 16, v28 bitop3:0x26
	v_bitop3_b32 v28, s39, v28, 24 bitop3:0xde
	v_and_or_b32 v30, v27, 22, v24
	v_and_or_b32 v24, v28, 30, v24
	v_and_b32_e32 v179, 15, v0
	v_lshl_or_b32 v202, v30, 10, v29
	v_lshl_or_b32 v203, v24, 10, v29
	v_lshlrev_b32_e32 v24, 3, v28
	v_lshlrev_b32_e32 v29, 2, v0
	v_lshrrev_b32_e32 v198, 8, v0
	v_lshlrev_b32_e32 v25, 3, v25
	v_lshlrev_b32_e32 v26, 3, v26
	v_lshlrev_b32_e32 v27, 3, v27
	v_and_or_b32 v28, v24, s37, v31
	v_and_b32_e32 v24, 48, v0
	v_and_b32_e32 v29, 32, v29
	v_lshlrev_b32_e32 v30, 6, v179
	s_mov_b32 s29, 0
	v_and_b32_e32 v199, 63, v0
	v_and_or_b32 v25, v25, s36, v31
	v_and_or_b32 v26, v26, s37, v31
	v_bfe_u32 v200, v0, 6, 2
	v_and_or_b32 v27, v27, s36, v31
	v_lshlrev_b32_e32 v80, 14, v198
	v_bitop3_b32 v81, v30, v29, v24 bitop3:0x36
	v_lshlrev_b32_e32 v190, 12, v25
	v_mov_b32_e32 v191, v183
	v_lshl_add_u64 v[24:25], s[20:21], 0, v[190:191]
	v_lshl_add_u64 v[24:25], v[24:25], 0, v[182:183]
	v_lshlrev_b32_e32 v192, 12, v26
	v_mov_b32_e32 v193, v183
	global_load_dwordx4 v[54:57], v[24:25], off offset:16
	global_load_dwordx4 v[58:61], v[24:25], off
	v_lshl_add_u64 v[24:25], s[20:21], 0, v[192:193]
	v_lshl_add_u64 v[24:25], v[24:25], 0, v[182:183]
	v_lshlrev_b32_e32 v194, 11, v27
	v_mov_b32_e32 v195, v183
	global_load_dwordx4 v[62:65], v[24:25], off offset:16
	global_load_dwordx4 v[66:69], v[24:25], off
	v_lshl_add_u64 v[24:25], s[22:23], 0, v[194:195]
	v_lshlrev_b32_e32 v196, 11, v28
	v_mov_b32_e32 v197, v183
	v_lshl_add_u64 v[24:25], v[24:25], 0, v[14:15]
	v_lshl_add_u64 v[26:27], s[22:23], 0, v[196:197]
	v_lshl_add_u64 v[26:27], v[26:27], 0, v[14:15]
	global_load_dwordx4 v[70:73], v[24:25], off
	global_load_dwordx4 v[74:77], v[26:27], off
	s_add_i32 s33, s33, 64
	s_and_b32 s20, s33, 0x3c0
	s_lshl_b32 s0, s20, 2
	s_add_u32 s0, s25, s0
	s_addc_u32 s1, s26, 0
	v_lshl_add_u64 v[24:25], s[0:1], 0, v[180:181]
	v_lshl_add_u64 v[24:25], v[24:25], 0, v[182:183]
	s_lshl_b32 s20, s20, 1
	global_load_dwordx4 v[42:45], v[24:25], off offset:16
	global_load_dwordx4 v[46:49], v[24:25], off
	v_lshl_add_u64 v[24:25], s[0:1], 0, v[184:185]
	s_add_u32 s20, s27, s20
	v_lshl_add_u64 v[24:25], v[24:25], 0, v[182:183]
	s_addc_u32 s21, s28, 0
	global_load_dwordx4 v[34:37], v[24:25], off offset:16
	global_load_dwordx4 v[38:41], v[24:25], off
	v_lshl_add_u64 v[24:25], s[20:21], 0, v[186:187]
	v_lshl_add_u64 v[24:25], v[24:25], 0, v[14:15]
	v_lshl_add_u64 v[26:27], s[20:21], 0, v[188:189]
	v_lshl_add_u64 v[78:79], v[26:27], 0, v[14:15]
	global_load_dwordx4 v[30:33], v[24:25], off
	global_load_dwordx4 v[26:29], v[78:79], off
	s_waitcnt vmcnt(16)
	v_cvt_pk_bf16_f32 v6, v6, v7
	v_cvt_pk_bf16_f32 v7, v8, v9
	v_cvt_pk_bf16_f32 v8, v2, v3
	v_add_u32_e32 v2, 0, v208
	v_cvt_pk_bf16_f32 v9, v4, v5
	ds_write_b128 v2, v[6:9]
	s_waitcnt vmcnt(14)
	v_cvt_pk_bf16_f32 v2, v16, v17
	v_add_u32_e32 v6, 0, v205
	v_cvt_pk_bf16_f32 v3, v18, v19
	v_cvt_pk_bf16_f32 v4, v10, v11
	v_cvt_pk_bf16_f32 v5, v12, v13
	ds_write_b128 v6, v[2:5]
	v_add_u32_e32 v2, 0, v206
	s_waitcnt vmcnt(13)
	ds_write_b128 v2, v[20:23] offset:32768
	v_add_u32_e32 v2, 0, v207
	s_waitcnt vmcnt(12)
	ds_write_b128 v2, v[50:53] offset:32768
	s_waitcnt vmcnt(10)
	v_cvt_pk_bf16_f32 v2, v58, v59
	v_add_u32_e32 v6, 0, v204
	v_cvt_pk_bf16_f32 v3, v60, v61
	v_cvt_pk_bf16_f32 v4, v54, v55
	v_cvt_pk_bf16_f32 v5, v56, v57
	ds_write_b128 v6, v[2:5]
	s_waitcnt vmcnt(8)
	v_cvt_pk_bf16_f32 v2, v66, v67
	v_add_u32_e32 v6, 0, v201
	v_cvt_pk_bf16_f32 v3, v68, v69
	v_cvt_pk_bf16_f32 v4, v62, v63
	v_cvt_pk_bf16_f32 v5, v64, v65
	ds_write_b128 v6, v[2:5]
	v_add_u32_e32 v2, 0, v202
	s_waitcnt vmcnt(7)
	ds_write_b128 v2, v[70:73] offset:32768
	v_add_u32_e32 v2, 0, v203
	s_waitcnt vmcnt(6)
	ds_write_b128 v2, v[74:77] offset:32768
	v_lshl_add_u64 v[2:3], s[0:1], 0, v[190:191]
	v_lshl_add_u64 v[2:3], v[2:3], 0, v[182:183]
	global_load_dwordx4 v[6:9], v[2:3], off offset:16
	global_load_dwordx4 v[22:25], v[2:3], off
	v_lshl_add_u64 v[2:3], s[0:1], 0, v[192:193]
	v_lshl_add_u64 v[16:17], v[2:3], 0, v[182:183]
	global_load_dwordx4 v[2:5], v[16:17], off offset:16
	global_load_dwordx4 v[10:13], v[16:17], off
	v_lshl_add_u64 v[16:17], s[20:21], 0, v[194:195]
	v_lshl_add_u64 v[50:51], v[16:17], 0, v[14:15]
	v_lshl_add_u64 v[16:17], s[20:21], 0, v[196:197]
	v_lshl_add_u64 v[52:53], v[16:17], 0, v[14:15]
	global_load_dwordx4 v[18:21], v[50:51], off
	global_load_dwordx4 v[14:17], v[52:53], off
	v_lshlrev_b32_e32 v50, 13, v200
	s_cmp_lg_u32 0, -1
	s_cselect_b32 s0, 0, 0
	v_add3_u32 v209, v80, s0, v81
	s_add_i32 s0, s0, 0x8000
	v_add3_u32 v210, v50, s0, v81
	s_lshl_b32 s0, s30, 1
	s_add_i32 s31, s31, s0
	s_lshl_b32 s0, s2, 3
	s_add_i32 s0, s0, s31
	s_waitcnt lgkmcnt(0)
	s_and_b32 s0, s0, 15
	s_lshl_b32 s0, s0, 6
	s_add_i32 s22, s0, 0x80
	v_mov_b32_e32 v50, v183
	v_mov_b32_e32 v51, v183
	v_mov_b32_e32 v52, v183
	v_mov_b32_e32 v53, v183
	v_mov_b32_e32 v54, v183
	v_mov_b32_e32 v55, v183
	v_mov_b32_e32 v56, v183
	v_mov_b32_e32 v57, v183
	v_mov_b32_e32 v58, v183
	v_mov_b32_e32 v59, v183
	v_mov_b32_e32 v60, v183
	v_mov_b32_e32 v61, v183
	v_mov_b32_e32 v62, v183
	v_mov_b32_e32 v63, v183
	v_mov_b32_e32 v64, v183
	v_mov_b32_e32 v65, v183
	v_mov_b32_e32 v66, v183
	v_mov_b32_e32 v67, v183
	v_mov_b32_e32 v68, v183
	v_mov_b32_e32 v69, v183
	v_mov_b32_e32 v70, v183
	v_mov_b32_e32 v71, v183
	v_mov_b32_e32 v72, v183
	v_mov_b32_e32 v73, v183
	v_mov_b32_e32 v74, v183
	v_mov_b32_e32 v75, v183
	v_mov_b32_e32 v76, v183
	v_mov_b32_e32 v77, v183
	v_mov_b32_e32 v78, v183
	v_mov_b32_e32 v79, v183
	v_mov_b32_e32 v80, v183
	v_mov_b32_e32 v81, v183
	v_mov_b32_e32 v82, v183
	v_mov_b32_e32 v83, v183
	v_mov_b32_e32 v84, v183
	v_mov_b32_e32 v85, v183
	v_mov_b32_e32 v86, v183
	v_mov_b32_e32 v87, v183
	v_mov_b32_e32 v88, v183
	v_mov_b32_e32 v89, v183
	v_mov_b32_e32 v90, v183
	v_mov_b32_e32 v91, v183
	v_mov_b32_e32 v92, v183
	v_mov_b32_e32 v93, v183
	v_mov_b32_e32 v94, v183
	v_mov_b32_e32 v95, v183
	v_mov_b32_e32 v96, v183
	v_mov_b32_e32 v97, v183
	v_mov_b32_e32 v98, v183
	v_mov_b32_e32 v99, v183
	v_mov_b32_e32 v100, v183
	v_mov_b32_e32 v101, v183
	v_mov_b32_e32 v102, v183
	v_mov_b32_e32 v103, v183
	v_mov_b32_e32 v104, v183
	v_mov_b32_e32 v105, v183
	v_mov_b32_e32 v106, v183
	v_mov_b32_e32 v107, v183
	v_mov_b32_e32 v108, v183
	v_mov_b32_e32 v109, v183
	v_mov_b32_e32 v110, v183
	v_mov_b32_e32 v111, v183
	v_mov_b32_e32 v112, v183
	v_mov_b32_e32 v113, v183
	v_mov_b32_e32 v114, v183
	v_mov_b32_e32 v115, v183
	v_mov_b32_e32 v116, v183
	v_mov_b32_e32 v117, v183
	v_mov_b32_e32 v118, v183
	v_mov_b32_e32 v119, v183
	v_mov_b32_e32 v120, v183
	v_mov_b32_e32 v121, v183
	v_mov_b32_e32 v122, v183
	v_mov_b32_e32 v123, v183
	v_mov_b32_e32 v124, v183
	v_mov_b32_e32 v125, v183
	v_mov_b32_e32 v126, v183
	v_mov_b32_e32 v127, v183
	v_mov_b32_e32 v128, v183
	v_mov_b32_e32 v129, v183
	v_mov_b32_e32 v130, v183
	v_mov_b32_e32 v131, v183
	v_mov_b32_e32 v132, v183
	v_mov_b32_e32 v133, v183
	v_mov_b32_e32 v134, v183
	v_mov_b32_e32 v135, v183
	v_mov_b32_e32 v136, v183
	v_mov_b32_e32 v137, v183
	v_mov_b32_e32 v138, v183
	v_mov_b32_e32 v139, v183
	v_mov_b32_e32 v140, v183
	v_mov_b32_e32 v141, v183
	v_mov_b32_e32 v142, v183
	v_mov_b32_e32 v143, v183
	v_mov_b32_e32 v144, v183
	v_mov_b32_e32 v145, v183
	v_mov_b32_e32 v146, v183
	v_mov_b32_e32 v147, v183
	v_mov_b32_e32 v148, v183
	v_mov_b32_e32 v149, v183
	v_mov_b32_e32 v150, v183
	v_mov_b32_e32 v151, v183
	v_mov_b32_e32 v152, v183
	v_mov_b32_e32 v153, v183
	v_mov_b32_e32 v154, v183
	v_mov_b32_e32 v155, v183
	v_mov_b32_e32 v156, v183
	v_mov_b32_e32 v157, v183
	v_mov_b32_e32 v158, v183
	v_mov_b32_e32 v159, v183
	v_mov_b32_e32 v160, v183
	v_mov_b32_e32 v161, v183
	v_mov_b32_e32 v162, v183
	v_mov_b32_e32 v163, v183
	v_mov_b32_e32 v164, v183
	v_mov_b32_e32 v165, v183
	v_mov_b32_e32 v166, v183
	v_mov_b32_e32 v167, v183
	v_mov_b32_e32 v168, v183
	v_mov_b32_e32 v169, v183
	v_mov_b32_e32 v170, v183
	v_mov_b32_e32 v171, v183
	v_mov_b32_e32 v172, v183
	v_mov_b32_e32 v173, v183
	v_mov_b32_e32 v174, v183
	v_mov_b32_e32 v175, v183
	v_mov_b32_e32 v176, v183
	v_mov_b32_e32 v177, v183
	s_and_b32 s0, s29, 0x10000
	v_add_u32_e32 v211, s0, v209
	v_add_u32_e32 v242, s0, v210
	s_barrier
.LBB1_1:
	ds_read_b128 v[212:215], v242 offset:0
	ds_read_b128 v[216:219], v242 offset:0x800
	ds_read_b128 v[220:223], v242 offset:0x1000
	ds_read_b128 v[224:227], v242 offset:0x1800
	ds_read_b128 v[228:231], v211 offset:0
	ds_read_b128 v[232:235], v211 offset:0x800
	ds_read_b128 v[236:239], v211 offset:0x1000
	s_waitcnt lgkmcnt(2)
	v_mfma_f32_16x16x32_bf16 v[174:177], v[212:215], v[228:231], v[174:177]
	v_mfma_f32_16x16x32_bf16 v[170:173], v[216:219], v[228:231], v[170:173]
	v_mfma_f32_16x16x32_bf16 v[166:169], v[220:223], v[228:231], v[166:169]
	v_mfma_f32_16x16x32_bf16 v[162:165], v[224:227], v[228:231], v[162:165]
	ds_read_b128 v[228:231], v211 offset:0x1800
	s_waitcnt lgkmcnt(2)
	v_mfma_f32_16x16x32_bf16 v[158:161], v[212:215], v[232:235], v[158:161]
	v_mfma_f32_16x16x32_bf16 v[154:157], v[216:219], v[232:235], v[154:157]
	v_mfma_f32_16x16x32_bf16 v[150:153], v[220:223], v[232:235], v[150:153]
	v_mfma_f32_16x16x32_bf16 v[146:149], v[224:227], v[232:235], v[146:149]
	ds_read_b128 v[232:235], v211 offset:0x2000
	s_waitcnt lgkmcnt(2)
	v_mfma_f32_16x16x32_bf16 v[142:145], v[212:215], v[236:239], v[142:145]
	v_mfma_f32_16x16x32_bf16 v[138:141], v[216:219], v[236:239], v[138:141]
	v_mfma_f32_16x16x32_bf16 v[134:137], v[220:223], v[236:239], v[134:137]
	v_mfma_f32_16x16x32_bf16 v[130:133], v[224:227], v[236:239], v[130:133]
	ds_read_b128 v[236:239], v211 offset:0x2800
	s_waitcnt lgkmcnt(2)
	v_mfma_f32_16x16x32_bf16 v[126:129], v[212:215], v[228:231], v[126:129]
	v_mfma_f32_16x16x32_bf16 v[122:125], v[216:219], v[228:231], v[122:125]
	v_mfma_f32_16x16x32_bf16 v[118:121], v[220:223], v[228:231], v[118:121]
	v_mfma_f32_16x16x32_bf16 v[114:117], v[224:227], v[228:231], v[114:117]
	ds_read_b128 v[228:231], v211 offset:0x3000
	s_waitcnt lgkmcnt(2)
	v_mfma_f32_16x16x32_bf16 v[110:113], v[212:215], v[232:235], v[110:113]
	v_mfma_f32_16x16x32_bf16 v[106:109], v[216:219], v[232:235], v[106:109]
	v_mfma_f32_16x16x32_bf16 v[102:105], v[220:223], v[232:235], v[102:105]
	v_mfma_f32_16x16x32_bf16 v[98:101], v[224:227], v[232:235], v[98:101]
	ds_read_b128 v[232:235], v211 offset:0x3800
	s_waitcnt lgkmcnt(2)
	v_mfma_f32_16x16x32_bf16 v[94:97], v[212:215], v[236:239], v[94:97]
	v_mfma_f32_16x16x32_bf16 v[90:93], v[216:219], v[236:239], v[90:93]
	v_mfma_f32_16x16x32_bf16 v[86:89], v[220:223], v[236:239], v[86:89]
	v_mfma_f32_16x16x32_bf16 v[82:85], v[224:227], v[236:239], v[82:85]
	s_waitcnt lgkmcnt(1)
	v_mfma_f32_16x16x32_bf16 v[78:81], v[212:215], v[228:231], v[78:81]
	v_mfma_f32_16x16x32_bf16 v[74:77], v[216:219], v[228:231], v[74:77]
	v_mfma_f32_16x16x32_bf16 v[70:73], v[220:223], v[228:231], v[70:73]
	v_mfma_f32_16x16x32_bf16 v[66:69], v[224:227], v[228:231], v[66:69]
	s_waitcnt lgkmcnt(0)
	v_mfma_f32_16x16x32_bf16 v[62:65], v[212:215], v[232:235], v[62:65]
	v_mfma_f32_16x16x32_bf16 v[58:61], v[216:219], v[232:235], v[58:61]
	v_mfma_f32_16x16x32_bf16 v[54:57], v[220:223], v[232:235], v[54:57]
	v_mfma_f32_16x16x32_bf16 v[50:53], v[224:227], v[232:235], v[50:53]
	s_xor_b32 s0, s0, 0x10000
	s_and_b32 s1, s22, 0x3c0
	s_add_i32 s23, s0, 0
	s_lshl_b32 s0, s1, 2
	s_add_u32 s20, s25, s0
	s_waitcnt vmcnt(10)
	v_cvt_pk_bf16_f32 v46, v46, v47
	v_cvt_pk_bf16_f32 v47, v48, v49
	v_cvt_pk_bf16_f32 v48, v42, v43
	v_cvt_pk_bf16_f32 v49, v44, v45
	s_waitcnt vmcnt(8)
	v_cvt_pk_bf16_f32 v38, v38, v39
	v_cvt_pk_bf16_f32 v39, v40, v41
	v_cvt_pk_bf16_f32 v40, v34, v35
	v_add_u32_e32 v34, s23, v208
	s_addc_u32 s21, s26, 0
	s_lshl_b32 s0, s1, 1
	v_cvt_pk_bf16_f32 v41, v36, v37
	v_lshlrev_b32_e32 v182, 2, v178
	v_add_u32_e32 v35, s23, v205
	v_add_u32_e32 v36, s23, v206
	v_add_u32_e32 v37, s23, v207
	ds_write_b128 v34, v[46:49]
	ds_write_b128 v35, v[38:41]
	s_waitcnt vmcnt(7)
	ds_write_b128 v36, v[30:33] offset:32768
	s_waitcnt vmcnt(6)
	ds_write_b128 v37, v[26:29] offset:32768
	v_lshl_add_u64 v[26:27], s[20:21], 0, v[180:181]
	v_lshl_add_u64 v[28:29], s[20:21], 0, v[184:185]
	s_add_u32 s0, s27, s0
	v_lshl_add_u64 v[26:27], v[26:27], 0, v[182:183]
	v_lshl_add_u64 v[28:29], v[28:29], 0, v[182:183]
	s_addc_u32 s1, s28, 0
	v_lshlrev_b32_e32 v240, 1, v178
	v_mov_b32_e32 v241, v183
	global_load_dwordx4 v[42:45], v[26:27], off offset:16
	global_load_dwordx4 v[46:49], v[26:27], off
	global_load_dwordx4 v[34:37], v[28:29], off offset:16
	global_load_dwordx4 v[38:41], v[28:29], off
	v_lshl_add_u64 v[26:27], s[0:1], 0, v[186:187]
	v_lshl_add_u64 v[28:29], s[0:1], 0, v[188:189]
	v_lshl_add_u64 v[26:27], v[26:27], 0, v[240:241]
	v_lshl_add_u64 v[28:29], v[28:29], 0, v[240:241]
	global_load_dwordx4 v[30:33], v[26:27], off
	s_nop 0
	global_load_dwordx4 v[26:29], v[28:29], off
	ds_read_b128 v[212:215], v242 offset:0x400
	ds_read_b128 v[216:219], v242 offset:0xc00
	ds_read_b128 v[220:223], v242 offset:0x1400
	ds_read_b128 v[224:227], v242 offset:0x1c00
	ds_read_b128 v[228:231], v211 offset:0x400
	ds_read_b128 v[232:235], v211 offset:0xc00
	ds_read_b128 v[236:239], v211 offset:0x1400
	s_waitcnt lgkmcnt(2)
	v_mfma_f32_16x16x32_bf16 v[174:177], v[212:215], v[228:231], v[174:177]
	v_mfma_f32_16x16x32_bf16 v[170:173], v[216:219], v[228:231], v[170:173]
	v_mfma_f32_16x16x32_bf16 v[166:169], v[220:223], v[228:231], v[166:169]
	v_mfma_f32_16x16x32_bf16 v[162:165], v[224:227], v[228:231], v[162:165]
	ds_read_b128 v[228:231], v211 offset:0x1c00
	s_waitcnt lgkmcnt(2)
	v_mfma_f32_16x16x32_bf16 v[158:161], v[212:215], v[232:235], v[158:161]
	v_mfma_f32_16x16x32_bf16 v[154:157], v[216:219], v[232:235], v[154:157]
	v_mfma_f32_16x16x32_bf16 v[150:153], v[220:223], v[232:235], v[150:153]
	v_mfma_f32_16x16x32_bf16 v[146:149], v[224:227], v[232:235], v[146:149]
	ds_read_b128 v[232:235], v211 offset:0x2400
	s_waitcnt lgkmcnt(2)
	v_mfma_f32_16x16x32_bf16 v[142:145], v[212:215], v[236:239], v[142:145]
	v_mfma_f32_16x16x32_bf16 v[138:141], v[216:219], v[236:239], v[138:141]
	v_mfma_f32_16x16x32_bf16 v[134:137], v[220:223], v[236:239], v[134:137]
	v_mfma_f32_16x16x32_bf16 v[130:133], v[224:227], v[236:239], v[130:133]
	ds_read_b128 v[236:239], v211 offset:0x2c00
	s_waitcnt lgkmcnt(2)
	v_mfma_f32_16x16x32_bf16 v[126:129], v[212:215], v[228:231], v[126:129]
	v_mfma_f32_16x16x32_bf16 v[122:125], v[216:219], v[228:231], v[122:125]
	v_mfma_f32_16x16x32_bf16 v[118:121], v[220:223], v[228:231], v[118:121]
	v_mfma_f32_16x16x32_bf16 v[114:117], v[224:227], v[228:231], v[114:117]
	ds_read_b128 v[228:231], v211 offset:0x3400
	s_waitcnt lgkmcnt(2)
	v_mfma_f32_16x16x32_bf16 v[110:113], v[212:215], v[232:235], v[110:113]
	v_mfma_f32_16x16x32_bf16 v[106:109], v[216:219], v[232:235], v[106:109]
	v_mfma_f32_16x16x32_bf16 v[102:105], v[220:223], v[232:235], v[102:105]
	v_mfma_f32_16x16x32_bf16 v[98:101], v[224:227], v[232:235], v[98:101]
	ds_read_b128 v[232:235], v211 offset:0x3c00
	s_waitcnt lgkmcnt(2)
	v_mfma_f32_16x16x32_bf16 v[94:97], v[212:215], v[236:239], v[94:97]
	v_mfma_f32_16x16x32_bf16 v[90:93], v[216:219], v[236:239], v[90:93]
	v_mfma_f32_16x16x32_bf16 v[86:89], v[220:223], v[236:239], v[86:89]
	v_mfma_f32_16x16x32_bf16 v[82:85], v[224:227], v[236:239], v[82:85]
	s_waitcnt lgkmcnt(1)
	v_mfma_f32_16x16x32_bf16 v[78:81], v[212:215], v[228:231], v[78:81]
	v_mfma_f32_16x16x32_bf16 v[74:77], v[216:219], v[228:231], v[74:77]
	v_mfma_f32_16x16x32_bf16 v[70:73], v[220:223], v[228:231], v[70:73]
	v_mfma_f32_16x16x32_bf16 v[66:69], v[224:227], v[228:231], v[66:69]
	s_waitcnt lgkmcnt(0)
	v_mfma_f32_16x16x32_bf16 v[62:65], v[212:215], v[232:235], v[62:65]
	v_mfma_f32_16x16x32_bf16 v[58:61], v[216:219], v[232:235], v[58:61]
	v_mfma_f32_16x16x32_bf16 v[54:57], v[220:223], v[232:235], v[54:57]
	v_mfma_f32_16x16x32_bf16 v[50:53], v[224:227], v[232:235], v[50:53]
	s_waitcnt vmcnt(10)
	v_cvt_pk_bf16_f32 v22, v22, v23
	v_cvt_pk_bf16_f32 v23, v24, v25
	v_cvt_pk_bf16_f32 v24, v6, v7
	v_cvt_pk_bf16_f32 v25, v8, v9
	v_add_u32_e32 v6, s23, v204
	s_waitcnt vmcnt(9)
	v_cvt_pk_bf16_f32 v8, v2, v3
	v_add_u32_e32 v2, s23, v201
	ds_write_b128 v6, v[22:25]
	s_waitcnt vmcnt(8)
	v_cvt_pk_bf16_f32 v6, v10, v11
	v_cvt_pk_bf16_f32 v7, v12, v13
	v_cvt_pk_bf16_f32 v9, v4, v5
	ds_write_b128 v2, v[6:9]
	v_add_u32_e32 v2, s23, v202
	s_waitcnt vmcnt(7)
	ds_write_b128 v2, v[18:21] offset:32768
	v_add_u32_e32 v2, s23, v203
	s_waitcnt vmcnt(6)
	ds_write_b128 v2, v[14:17] offset:32768
	v_lshl_add_u64 v[2:3], s[20:21], 0, v[190:191]
	v_lshl_add_u64 v[2:3], v[2:3], 0, v[182:183]
	global_load_dwordx4 v[6:9], v[2:3], off offset:16
	global_load_dwordx4 v[22:25], v[2:3], off
	v_lshl_add_u64 v[2:3], s[20:21], 0, v[192:193]
	v_lshl_add_u64 v[14:15], s[0:1], 0, v[194:195]
	v_lshl_add_u64 v[16:17], s[0:1], 0, v[196:197]
	v_lshl_add_u64 v[10:11], v[2:3], 0, v[182:183]
	v_lshl_add_u64 v[14:15], v[14:15], 0, v[240:241]
	v_lshl_add_u64 v[16:17], v[16:17], 0, v[240:241]
	global_load_dwordx4 v[2:5], v[10:11], off offset:16
	s_nop 0
	global_load_dwordx4 v[10:13], v[10:11], off
	s_nop 0
	global_load_dwordx4 v[18:21], v[14:15], off
	s_nop 0
	global_load_dwordx4 v[14:17], v[16:17], off
	s_waitcnt lgkmcnt(0)
	s_add_i32 s22, s22, 64
	s_add_i32 s29, s29, 0x10000
	s_and_b32 s0, s29, 0x10000
	v_add_u32_e32 v211, s0, v209
	v_add_u32_e32 v242, s0, v210
	s_cmp_lg_u32 s29, 0xe0000
	s_barrier
	s_cbranch_scc1 .LBB1_1
	s_lshl_b64 s[0:1], s[18:19], 24
	ds_read_b128 v[180:183], v210 offset:0
	ds_read_b128 v[184:187], v210 offset:0x800
	ds_read_b128 v[188:191], v210 offset:0x1000
	ds_read_b128 v[192:195], v210 offset:0x1800
	ds_read_b128 v[212:215], v209 offset:0
	ds_read_b128 v[216:219], v209 offset:0x800
	ds_read_b128 v[220:223], v209 offset:0x1000
	s_waitcnt lgkmcnt(0)
	s_add_u32 s0, s10, s0
	s_addc_u32 s18, s11, s1
	s_lshl_b32 s19, s24, 1
	s_mov_b32 s1, 0
	s_add_u32 s0, s0, s19
	s_waitcnt lgkmcnt(2)
	s_addc_u32 s20, s18, 0
	v_mfma_f32_16x16x32_bf16 v[174:177], v[180:183], v[212:215], v[174:177]
	v_mfma_f32_16x16x32_bf16 v[170:173], v[184:187], v[212:215], v[170:173]
	v_mfma_f32_16x16x32_bf16 v[166:169], v[188:191], v[212:215], v[166:169]
	v_mfma_f32_16x16x32_bf16 v[162:165], v[192:195], v[212:215], v[162:165]
	ds_read_b128 v[212:215], v209 offset:0x1800
	s_waitcnt lgkmcnt(2)
	s_nop 0
	v_mfma_f32_16x16x32_bf16 v[158:161], v[180:183], v[216:219], v[158:161]
	v_mfma_f32_16x16x32_bf16 v[154:157], v[184:187], v[216:219], v[154:157]
	v_mfma_f32_16x16x32_bf16 v[150:153], v[188:191], v[216:219], v[150:153]
	v_mfma_f32_16x16x32_bf16 v[146:149], v[192:195], v[216:219], v[146:149]
	ds_read_b128 v[216:219], v209 offset:0x2000
	s_waitcnt lgkmcnt(2)
	s_nop 0
	v_mfma_f32_16x16x32_bf16 v[142:145], v[180:183], v[220:223], v[142:145]
	v_mfma_f32_16x16x32_bf16 v[138:141], v[184:187], v[220:223], v[138:141]
	v_mfma_f32_16x16x32_bf16 v[134:137], v[188:191], v[220:223], v[134:137]
	v_mfma_f32_16x16x32_bf16 v[130:133], v[192:195], v[220:223], v[130:133]
	ds_read_b128 v[220:223], v209 offset:0x2800
	s_waitcnt lgkmcnt(2)
	s_nop 0
	v_mfma_f32_16x16x32_bf16 v[126:129], v[180:183], v[212:215], v[126:129]
	v_mfma_f32_16x16x32_bf16 v[122:125], v[184:187], v[212:215], v[122:125]
	v_mfma_f32_16x16x32_bf16 v[118:121], v[188:191], v[212:215], v[118:121]
	v_mfma_f32_16x16x32_bf16 v[114:117], v[192:195], v[212:215], v[114:117]
	ds_read_b128 v[212:215], v209 offset:0x3000
	s_waitcnt lgkmcnt(2)
	s_nop 0
	v_mfma_f32_16x16x32_bf16 v[110:113], v[180:183], v[216:219], v[110:113]
	v_mfma_f32_16x16x32_bf16 v[106:109], v[184:187], v[216:219], v[106:109]
	v_mfma_f32_16x16x32_bf16 v[102:105], v[188:191], v[216:219], v[102:105]
	v_mfma_f32_16x16x32_bf16 v[98:101], v[192:195], v[216:219], v[98:101]
	ds_read_b128 v[216:219], v209 offset:0x3800
	s_waitcnt lgkmcnt(2)
	s_nop 0
	v_mfma_f32_16x16x32_bf16 v[94:97], v[180:183], v[220:223], v[94:97]
	v_mfma_f32_16x16x32_bf16 v[90:93], v[184:187], v[220:223], v[90:93]
	v_mfma_f32_16x16x32_bf16 v[86:89], v[188:191], v[220:223], v[86:89]
	v_mfma_f32_16x16x32_bf16 v[82:85], v[192:195], v[220:223], v[82:85]
	s_waitcnt lgkmcnt(1)
	s_nop 0
	v_mfma_f32_16x16x32_bf16 v[78:81], v[180:183], v[212:215], v[78:81]
	v_mfma_f32_16x16x32_bf16 v[74:77], v[184:187], v[212:215], v[74:77]
	v_mfma_f32_16x16x32_bf16 v[70:73], v[188:191], v[212:215], v[70:73]
	v_mfma_f32_16x16x32_bf16 v[66:69], v[192:195], v[212:215], v[66:69]
	s_waitcnt lgkmcnt(0)
	s_nop 0
	v_mfma_f32_16x16x32_bf16 v[62:65], v[180:183], v[216:219], v[62:65]
	v_mfma_f32_16x16x32_bf16 v[58:61], v[184:187], v[216:219], v[58:61]
	v_mfma_f32_16x16x32_bf16 v[54:57], v[188:191], v[216:219], v[54:57]
	v_mfma_f32_16x16x32_bf16 v[50:53], v[192:195], v[216:219], v[50:53]
	s_add_i32 s18, 0, 0x10000
	s_waitcnt vmcnt(10)
	v_cvt_pk_bf16_f32 v46, v46, v47
	v_cvt_pk_bf16_f32 v47, v48, v49
	v_cvt_pk_bf16_f32 v48, v42, v43
	v_add_u32_e32 v42, s18, v208
	s_waitcnt vmcnt(8)
	v_cvt_pk_bf16_f32 v38, v38, v39
	v_cvt_pk_bf16_f32 v39, v40, v41
	v_cvt_pk_bf16_f32 v40, v34, v35
	v_add_u32_e32 v34, s18, v205
	s_add_i32 s19, 0, 0x18000
	v_cvt_pk_bf16_f32 v49, v44, v45
	ds_write_b128 v42, v[46:49]
	v_cvt_pk_bf16_f32 v41, v36, v37
	ds_write_b128 v34, v[38:41]
	v_add_u32_e32 v34, s19, v206
	s_waitcnt vmcnt(7)
	ds_write_b128 v34, v[30:33]
	v_add_u32_e32 v30, s19, v207
	s_waitcnt vmcnt(6)
	ds_write_b128 v30, v[26:29]
	ds_read_b128 v[26:29], v210 offset:0x400
	ds_read_b128 v[30:33], v210 offset:0xc00
	ds_read_b128 v[34:37], v210 offset:0x1400
	ds_read_b128 v[38:41], v210 offset:0x1c00
	ds_read_b128 v[42:45], v209 offset:0x400
	ds_read_b128 v[46:49], v209 offset:0xc00
	ds_read_b128 v[180:183], v209 offset:0x1400
	s_nop 0
	s_waitcnt lgkmcnt(2)
	s_nop 0
	v_mfma_f32_16x16x32_bf16 v[174:177], v[26:29], v[42:45], v[174:177]
	v_mfma_f32_16x16x32_bf16 v[170:173], v[30:33], v[42:45], v[170:173]
	v_mfma_f32_16x16x32_bf16 v[166:169], v[34:37], v[42:45], v[166:169]
	v_mfma_f32_16x16x32_bf16 v[42:45], v[38:41], v[42:45], v[162:165]
	ds_read_b128 v[162:165], v209 offset:0x1c00
	s_waitcnt lgkmcnt(2)
	s_nop 0
	v_mfma_f32_16x16x32_bf16 v[158:161], v[26:29], v[46:49], v[158:161]
	v_mfma_f32_16x16x32_bf16 v[154:157], v[30:33], v[46:49], v[154:157]
	v_mfma_f32_16x16x32_bf16 v[150:153], v[34:37], v[46:49], v[150:153]
	v_mfma_f32_16x16x32_bf16 v[46:49], v[38:41], v[46:49], v[146:149]
	ds_read_b128 v[146:149], v209 offset:0x2400
	s_waitcnt lgkmcnt(2)
	s_nop 0
	v_mfma_f32_16x16x32_bf16 v[142:145], v[26:29], v[180:183], v[142:145]
	v_mfma_f32_16x16x32_bf16 v[138:141], v[30:33], v[180:183], v[138:141]
	v_mfma_f32_16x16x32_bf16 v[134:137], v[34:37], v[180:183], v[134:137]
	v_mfma_f32_16x16x32_bf16 v[130:133], v[38:41], v[180:183], v[130:133]
	ds_read_b128 v[180:183], v209 offset:0x2c00
	s_waitcnt lgkmcnt(2)
	s_nop 0
	v_mfma_f32_16x16x32_bf16 v[126:129], v[26:29], v[162:165], v[126:129]
	v_mfma_f32_16x16x32_bf16 v[122:125], v[30:33], v[162:165], v[122:125]
	v_mfma_f32_16x16x32_bf16 v[118:121], v[34:37], v[162:165], v[118:121]
	v_mfma_f32_16x16x32_bf16 v[114:117], v[38:41], v[162:165], v[114:117]
	ds_read_b128 v[162:165], v209 offset:0x3400
	s_waitcnt lgkmcnt(2)
	s_nop 0
	v_mfma_f32_16x16x32_bf16 v[110:113], v[26:29], v[146:149], v[110:113]
	v_mfma_f32_16x16x32_bf16 v[106:109], v[30:33], v[146:149], v[106:109]
	v_mfma_f32_16x16x32_bf16 v[102:105], v[34:37], v[146:149], v[102:105]
	v_mfma_f32_16x16x32_bf16 v[98:101], v[38:41], v[146:149], v[98:101]
	ds_read_b128 v[146:149], v209 offset:0x3c00
	s_waitcnt lgkmcnt(2)
	s_nop 0
	v_mfma_f32_16x16x32_bf16 v[94:97], v[26:29], v[180:183], v[94:97]
	v_mfma_f32_16x16x32_bf16 v[90:93], v[30:33], v[180:183], v[90:93]
	v_mfma_f32_16x16x32_bf16 v[86:89], v[34:37], v[180:183], v[86:89]
	v_mfma_f32_16x16x32_bf16 v[82:85], v[38:41], v[180:183], v[82:85]
	s_waitcnt lgkmcnt(1)
	s_nop 0
	v_mfma_f32_16x16x32_bf16 v[78:81], v[26:29], v[162:165], v[78:81]
	v_mfma_f32_16x16x32_bf16 v[74:77], v[30:33], v[162:165], v[74:77]
	v_mfma_f32_16x16x32_bf16 v[70:73], v[34:37], v[162:165], v[70:73]
	v_mfma_f32_16x16x32_bf16 v[66:69], v[38:41], v[162:165], v[66:69]
	s_waitcnt lgkmcnt(0)
	s_nop 0
	v_mfma_f32_16x16x32_bf16 v[26:29], v[26:29], v[146:149], v[62:65]
	v_mfma_f32_16x16x32_bf16 v[30:33], v[30:33], v[146:149], v[58:61]
	v_mfma_f32_16x16x32_bf16 v[34:37], v[34:37], v[146:149], v[54:57]
	v_mfma_f32_16x16x32_bf16 v[38:41], v[38:41], v[146:149], v[50:53]
	s_waitcnt vmcnt(4)
	v_cvt_pk_bf16_f32 v22, v22, v23
	v_cvt_pk_bf16_f32 v23, v24, v25
	v_cvt_pk_bf16_f32 v24, v6, v7
	v_cvt_pk_bf16_f32 v25, v8, v9
	v_add_u32_e32 v6, s18, v204
	s_waitcnt vmcnt(3)
	v_cvt_pk_bf16_f32 v8, v2, v3
	v_add_u32_e32 v2, s18, v201
	ds_write_b128 v6, v[22:25]
	s_waitcnt vmcnt(2)
	v_cvt_pk_bf16_f32 v6, v10, v11
	v_cvt_pk_bf16_f32 v7, v12, v13
	v_cvt_pk_bf16_f32 v9, v4, v5
	ds_write_b128 v2, v[6:9]
	v_add_u32_e32 v2, s19, v202
	s_waitcnt vmcnt(1)
	ds_write_b128 v2, v[18:21]
	v_add_u32_e32 v2, s19, v203
	s_waitcnt vmcnt(0)
	ds_write_b128 v2, v[14:17]
	s_waitcnt lgkmcnt(0)
	s_barrier
	v_add_u32_e32 v178, 0x10000, v209
	v_add_u32_e32 v196, 0x10000, v210
	ds_read_b128 v[2:5], v196 offset:0
	ds_read_b128 v[6:9], v196 offset:0x800
	ds_read_b128 v[10:13], v196 offset:0x1000
	ds_read_b128 v[14:17], v196 offset:0x1800
	ds_read_b128 v[18:21], v178 offset:0
	s_and_b64 s[16:17], s[16:17], exec
	ds_read_b128 v[22:25], v178 offset:0x800
	ds_read_b128 v[50:53], v178 offset:0x1000
	s_waitcnt lgkmcnt(2)
	s_cselect_b32 s5, s5, s7
	s_cselect_b32 s4, s4, s6
	s_lshl_b32 s6, s3, 10
	v_mfma_f32_16x16x32_bf16 v[54:57], v[2:5], v[18:21], v[174:177]
	s_add_u32 s6, s4, s6
	s_addc_u32 s7, s5, 0
	s_lshl_b32 s3, s3, 9
	v_mfma_f32_16x16x32_bf16 v[58:61], v[6:9], v[18:21], v[170:173]
	s_add_u32 s4, s0, s3
	s_addc_u32 s5, s20, 0
	v_mfma_f32_16x16x32_bf16 v[62:65], v[10:13], v[18:21], v[166:169]
	v_mfma_f32_16x16x32_bf16 v[18:21], v[14:17], v[18:21], v[42:45]
	ds_read_b128 v[42:45], v178 offset:0x1800
	s_waitcnt lgkmcnt(2)
	s_nop 0
	v_mfma_f32_16x16x32_bf16 v[146:149], v[2:5], v[22:25], v[158:161]
	v_mfma_f32_16x16x32_bf16 v[154:157], v[6:9], v[22:25], v[154:157]
	v_mfma_f32_16x16x32_bf16 v[150:153], v[10:13], v[22:25], v[150:153]
	v_mfma_f32_16x16x32_bf16 v[22:25], v[14:17], v[22:25], v[46:49]
	ds_read_b128 v[46:49], v178 offset:0x2000
	s_waitcnt lgkmcnt(2)
	s_nop 0
	v_mfma_f32_16x16x32_bf16 v[142:145], v[2:5], v[50:53], v[142:145]
	v_mfma_f32_16x16x32_bf16 v[138:141], v[6:9], v[50:53], v[138:141]
	v_mfma_f32_16x16x32_bf16 v[134:137], v[10:13], v[50:53], v[134:137]
	v_mfma_f32_16x16x32_bf16 v[50:53], v[14:17], v[50:53], v[130:133]
	ds_read_b128 v[130:133], v178 offset:0x2800
	s_waitcnt lgkmcnt(2)
	s_nop 0
	v_mfma_f32_16x16x32_bf16 v[126:129], v[2:5], v[42:45], v[126:129]
	v_mfma_f32_16x16x32_bf16 v[122:125], v[6:9], v[42:45], v[122:125]
	v_mfma_f32_16x16x32_bf16 v[118:121], v[10:13], v[42:45], v[118:121]
	v_mfma_f32_16x16x32_bf16 v[42:45], v[14:17], v[42:45], v[114:117]
	ds_read_b128 v[114:117], v178 offset:0x3000
	s_waitcnt lgkmcnt(2)
	s_nop 0
	v_mfma_f32_16x16x32_bf16 v[110:113], v[2:5], v[46:49], v[110:113]
	v_mfma_f32_16x16x32_bf16 v[106:109], v[6:9], v[46:49], v[106:109]
	v_mfma_f32_16x16x32_bf16 v[102:105], v[10:13], v[46:49], v[102:105]
	v_mfma_f32_16x16x32_bf16 v[98:101], v[14:17], v[46:49], v[98:101]
	ds_read_b128 v[46:49], v178 offset:0x3800
	s_waitcnt lgkmcnt(2)
	s_nop 0
	v_mfma_f32_16x16x32_bf16 v[158:161], v[2:5], v[130:133], v[94:97]
	v_mfma_f32_16x16x32_bf16 v[162:165], v[6:9], v[130:133], v[90:93]
	v_mfma_f32_16x16x32_bf16 v[166:169], v[10:13], v[130:133], v[86:89]
	v_mfma_f32_16x16x32_bf16 v[130:133], v[14:17], v[130:133], v[82:85]
	s_waitcnt lgkmcnt(1)
	s_nop 0
	v_mfma_f32_16x16x32_bf16 v[66:69], v[14:17], v[114:117], v[66:69]
	v_mfma_f32_16x16x32_bf16 v[170:173], v[2:5], v[114:117], v[78:81]
	v_mfma_f32_16x16x32_bf16 v[174:177], v[6:9], v[114:117], v[74:77]
	v_mfma_f32_16x16x32_bf16 v[180:183], v[10:13], v[114:117], v[70:73]
	s_waitcnt lgkmcnt(0)
	s_nop 0
	v_mfma_f32_16x16x32_bf16 v[2:5], v[2:5], v[46:49], v[26:29]
	v_mfma_f32_16x16x32_bf16 v[114:117], v[6:9], v[46:49], v[30:33]
	v_mfma_f32_16x16x32_bf16 v[34:37], v[10:13], v[46:49], v[34:37]
	v_mfma_f32_16x16x32_bf16 v[184:187], v[14:17], v[46:49], v[38:41]
	ds_read_b128 v[188:191], v196 offset:0x400
	ds_read_b128 v[192:195], v196 offset:0xc00
	ds_read_b128 v[202:205], v196 offset:0x1400
	ds_read_b128 v[206:209], v196 offset:0x1c00
	ds_read_b128 v[6:9], v178 offset:0x400
	ds_read_b128 v[10:13], v178 offset:0xc00
	ds_read_b128 v[14:17], v178 offset:0x1400
	s_nop 0
	s_waitcnt lgkmcnt(2)
	s_nop 0
	v_mfma_f32_16x16x32_bf16 v[94:97], v[192:195], v[6:9], v[58:61]
	v_mfma_f32_16x16x32_bf16 v[62:65], v[202:205], v[6:9], v[62:65]
	v_mfma_f32_16x16x32_bf16 v[30:33], v[206:209], v[6:9], v[18:21]
	v_mfma_f32_16x16x32_bf16 v[210:213], v[188:191], v[6:9], v[54:57]
	ds_read_b128 v[6:9], v178 offset:0x1c00
	s_waitcnt lgkmcnt(2)
	s_nop 0
	v_mfma_f32_16x16x32_bf16 v[90:93], v[192:195], v[10:13], v[154:157]
	v_mfma_f32_16x16x32_bf16 v[58:61], v[202:205], v[10:13], v[150:153]
	v_mfma_f32_16x16x32_bf16 v[26:29], v[206:209], v[10:13], v[22:25]
	v_mfma_f32_16x16x32_bf16 v[146:149], v[188:191], v[10:13], v[146:149]
	ds_read_b128 v[10:13], v178 offset:0x2400
	s_waitcnt lgkmcnt(2)
	s_nop 0
	v_mfma_f32_16x16x32_bf16 v[86:89], v[192:195], v[14:17], v[138:141]
	v_mfma_f32_16x16x32_bf16 v[54:57], v[202:205], v[14:17], v[134:137]
	v_mfma_f32_16x16x32_bf16 v[22:25], v[206:209], v[14:17], v[50:53]
	v_mfma_f32_16x16x32_bf16 v[142:145], v[188:191], v[14:17], v[142:145]
	ds_read_b128 v[38:41], v178 offset:0x2c00
	s_waitcnt lgkmcnt(2)
	s_nop 0
	v_mfma_f32_16x16x32_bf16 v[126:129], v[188:191], v[6:9], v[126:129]
	v_mfma_f32_16x16x32_bf16 v[82:85], v[192:195], v[6:9], v[122:125]
	v_mfma_f32_16x16x32_bf16 v[50:53], v[202:205], v[6:9], v[118:121]
	v_mfma_f32_16x16x32_bf16 v[18:21], v[206:209], v[6:9], v[42:45]
	ds_read_b128 v[6:9], v178 offset:0x3400
	s_waitcnt lgkmcnt(2)
	s_nop 0
	v_mfma_f32_16x16x32_bf16 v[110:113], v[188:191], v[10:13], v[110:113]
	v_mfma_f32_16x16x32_bf16 v[78:81], v[192:195], v[10:13], v[106:109]
	v_mfma_f32_16x16x32_bf16 v[46:49], v[202:205], v[10:13], v[102:105]
	v_mfma_f32_16x16x32_bf16 v[14:17], v[206:209], v[10:13], v[98:101]
	ds_read_b128 v[98:101], v178 offset:0x3c00
	s_waitcnt lgkmcnt(2)
	s_nop 0
	v_mfma_f32_16x16x32_bf16 v[106:109], v[188:191], v[38:41], v[158:161]
	v_mfma_f32_16x16x32_bf16 v[74:77], v[192:195], v[38:41], v[162:165]
	v_mfma_f32_16x16x32_bf16 v[42:45], v[202:205], v[38:41], v[166:169]
	v_mfma_f32_16x16x32_bf16 v[10:13], v[206:209], v[38:41], v[130:133]
	s_waitcnt lgkmcnt(1)
	s_nop 0
	v_mfma_f32_16x16x32_bf16 v[118:121], v[188:191], v[6:9], v[170:173]
	v_mfma_f32_16x16x32_bf16 v[70:73], v[192:195], v[6:9], v[174:177]
	v_mfma_f32_16x16x32_bf16 v[38:41], v[202:205], v[6:9], v[180:183]
	v_mfma_f32_16x16x32_bf16 v[6:9], v[206:209], v[6:9], v[66:69]
	s_waitcnt lgkmcnt(0)
	s_nop 0
	v_mfma_f32_16x16x32_bf16 v[122:125], v[188:191], v[98:101], v[2:5]
	v_mfma_f32_16x16x32_bf16 v[66:69], v[192:195], v[98:101], v[114:117]
	v_mfma_f32_16x16x32_bf16 v[34:37], v[202:205], v[98:101], v[34:37]
	v_mfma_f32_16x16x32_bf16 v[2:5], v[206:209], v[98:101], v[184:187]
	v_lshrrev_b32_e32 v98, 2, v199
	v_and_b32_e32 v98, 12, v98
	v_lshl_or_b32 v104, v200, 6, v98
	v_lshlrev_b32_e32 v105, 2, v104
	s_waitcnt lgkmcnt(0)
	s_barrier
	global_load_dwordx4 v[114:117], v105, s[6:7]
	v_lshrrev_b32_e32 v98, 1, v199
	v_lshlrev_b32_e32 v99, 16, v198
	v_lshlrev_b32_e32 v100, 9, v179
	v_and_b32_e32 v102, 8, v98
	v_lshrrev_b32_e32 v98, 3, v104
	v_add3_u32 v103, 0, v99, v100
	v_xor_b32_e32 v130, v98, v179
	v_bitop3_b32 v131, v98, v179, 16 bitop3:0x1e
	global_load_dwordx4 v[98:101], v105, s[6:7] offset:64
	v_lshlrev_b32_e32 v130, 4, v130
	v_lshlrev_b32_e32 v131, 4, v131
	v_add3_u32 v130, v103, v130, v102
	v_add3_u32 v131, v103, v131, v102
	s_movk_i32 s0, 0x200
	s_waitcnt vmcnt(1)
	v_add_f32_e32 v132, v210, v114
	v_add_f32_e32 v133, v211, v115
	v_add_f32_e32 v134, v212, v116
	v_add_f32_e32 v135, v213, v117
	v_add_f32_e32 v140, v142, v114
	v_add_f32_e32 v141, v143, v115
	v_add_f32_e32 v142, v144, v116
	v_add_f32_e32 v143, v145, v117
	v_add_f32_e32 v110, v110, v114
	v_add_f32_e32 v111, v111, v115
	v_add_f32_e32 v106, v106, v114
	v_add_f32_e32 v107, v107, v115
	v_add_f32_e32 v136, v146, v114
	v_add_f32_e32 v137, v147, v115
	v_add_f32_e32 v138, v148, v116
	v_add_f32_e32 v139, v149, v117
	v_add_f32_e32 v126, v126, v114
	v_add_f32_e32 v127, v127, v115
	v_add_f32_e32 v128, v128, v116
	v_add_f32_e32 v129, v129, v117
	v_add_f32_e32 v112, v112, v116
	v_add_f32_e32 v113, v113, v117
	v_add_f32_e32 v108, v108, v116
	v_add_f32_e32 v109, v109, v117
	v_max_f32_e32 v132, 0, v132
	v_max_f32_e32 v133, 0, v133
	v_max_f32_e32 v134, 0, v134
	v_max_f32_e32 v135, 0, v135
	v_max_f32_e32 v140, 0, v140
	v_max_f32_e32 v141, 0, v141
	v_max_f32_e32 v142, 0, v142
	v_max_f32_e32 v143, 0, v143
	v_max_f32_e32 v144, 0, v110
	v_max_f32_e32 v145, 0, v111
	v_max_f32_e32 v148, 0, v106
	v_max_f32_e32 v149, 0, v107
	v_cvt_pk_bf16_f32 v106, v132, v133
	v_cvt_pk_bf16_f32 v107, v134, v135
	v_cvt_pk_bf16_f32 v110, v140, v141
	v_cvt_pk_bf16_f32 v111, v142, v143
	v_add_f32_e32 v118, v118, v114
	v_add_f32_e32 v119, v119, v115
	v_max_f32_e32 v136, 0, v136
	v_max_f32_e32 v137, 0, v137
	v_max_f32_e32 v138, 0, v138
	v_max_f32_e32 v139, 0, v139
	v_max_f32_e32 v126, 0, v126
	v_max_f32_e32 v127, 0, v127
	v_max_f32_e32 v128, 0, v128
	v_max_f32_e32 v129, 0, v129
	v_max_f32_e32 v146, 0, v112
	v_max_f32_e32 v147, 0, v113
	v_max_f32_e32 v150, 0, v108
	v_max_f32_e32 v151, 0, v109
	v_cvt_pk_bf16_f32 v108, v136, v137
	v_cvt_pk_bf16_f32 v109, v138, v139
	v_cvt_pk_bf16_f32 v112, v126, v127
	v_cvt_pk_bf16_f32 v113, v128, v129
	ds_write2st64_b64 v130, v[106:107], v[110:111] offset1:32
	ds_write2st64_b64 v131, v[108:109], v[112:113] offset0:16 offset1:48
	v_add_f32_e32 v106, v121, v117
	v_add_f32_e32 v120, v120, v116
	v_max_f32_e32 v152, 0, v118
	v_max_f32_e32 v153, 0, v119
	v_max_f32_e32 v107, 0, v106
	v_cvt_pk_bf16_f32 v106, v152, v153
	v_max_f32_e32 v120, 0, v120
	v_cvt_pk_bf16_f32 v118, v144, v145
	v_cvt_pk_bf16_f32 v119, v146, v147
	v_cvt_pk_bf16_f32 v107, v120, v107
	ds_write2st64_b64 v130, v[118:119], v[106:107] offset0:64 offset1:96
	v_add_f32_e32 v106, v122, v114
	v_max_f32_e32 v106, 0, v106
	v_add_f32_e32 v107, v123, v115
	v_max_f32_e32 v107, 0, v107
	v_add_f32_e32 v108, v124, v116
	v_add_f32_e32 v109, v125, v117
	v_cvt_pk_bf16_f32 v106, v106, v107
	v_cvt_pk_bf16_f32 v126, v148, v149
	v_cvt_pk_bf16_f32 v127, v150, v151
	v_max_f32_e32 v108, 0, v108
	v_max_f32_e32 v109, 0, v109
	v_cvt_pk_bf16_f32 v107, v108, v109
	ds_write2st64_b64 v131, v[126:127], v[106:107] offset0:80 offset1:112
	v_or_b32_e32 v106, 16, v104
	s_waitcnt vmcnt(0)
	v_add_f32_e32 v94, v94, v98
	v_add_f32_e32 v95, v95, v99
	v_add_f32_e32 v96, v96, v100
	v_lshrrev_b32_e32 v106, 3, v106
	v_max_f32_e32 v94, 0, v94
	v_max_f32_e32 v95, 0, v95
	v_max_f32_e32 v96, 0, v96
	v_add_f32_e32 v97, v97, v101
	v_max_f32_e32 v97, 0, v97
	v_cvt_pk_bf16_f32 v94, v94, v95
	v_cvt_pk_bf16_f32 v95, v96, v97
	v_xor_b32_e32 v96, v106, v179
	v_lshlrev_b32_e32 v96, 4, v96
	v_add3_u32 v107, v103, v96, v102
	v_add_f32_e32 v90, v90, v98
	v_add_f32_e32 v91, v91, v99
	v_add_f32_e32 v92, v92, v100
	ds_write_b64 v107, v[94:95]
	v_max_f32_e32 v90, 0, v90
	v_max_f32_e32 v91, 0, v91
	global_load_dwordx4 v[94:97], v105, s[6:7] offset:128
	v_max_f32_e32 v92, 0, v92
	v_add_f32_e32 v93, v93, v101
	v_max_f32_e32 v93, 0, v93
	v_cvt_pk_bf16_f32 v90, v90, v91
	v_cvt_pk_bf16_f32 v91, v92, v93
	v_bitop3_b32 v92, v106, v179, 16 bitop3:0x1e
	v_add_f32_e32 v66, v66, v98
	v_lshlrev_b32_e32 v92, 4, v92
	v_add_f32_e32 v86, v86, v98
	v_add_f32_e32 v87, v87, v99
	v_add_f32_e32 v82, v82, v98
	v_add_f32_e32 v83, v83, v99
	v_add_f32_e32 v78, v78, v98
	v_add_f32_e32 v79, v79, v99
	v_add_f32_e32 v74, v74, v98
	v_add_f32_e32 v75, v75, v99
	v_add_f32_e32 v70, v70, v98
	v_add_f32_e32 v71, v71, v99
	v_max_f32_e32 v66, 0, v66
	v_add_f32_e32 v67, v67, v99
	v_add3_u32 v92, v103, v92, v102
	v_max_f32_e32 v86, 0, v86
	v_max_f32_e32 v87, 0, v87
	v_add_f32_e32 v88, v88, v100
	v_add_f32_e32 v89, v89, v101
	v_max_f32_e32 v82, 0, v82
	v_max_f32_e32 v83, 0, v83
	v_add_f32_e32 v84, v84, v100
	v_add_f32_e32 v85, v85, v101
	v_max_f32_e32 v78, 0, v78
	v_max_f32_e32 v79, 0, v79
	v_add_f32_e32 v80, v80, v100
	v_add_f32_e32 v81, v81, v101
	v_max_f32_e32 v74, 0, v74
	v_max_f32_e32 v75, 0, v75
	v_add_f32_e32 v76, v76, v100
	v_add_f32_e32 v77, v77, v101
	v_max_f32_e32 v70, 0, v70
	v_max_f32_e32 v71, 0, v71
	v_add_f32_e32 v72, v72, v100
	v_add_f32_e32 v73, v73, v101
	v_max_f32_e32 v67, 0, v67
	v_add_f32_e32 v68, v68, v100
	v_add_f32_e32 v69, v69, v101
	v_cvt_pk_bf16_f32 v66, v66, v67
	ds_write_b64 v92, v[90:91] offset:8192
	v_max_f32_e32 v88, 0, v88
	v_max_f32_e32 v89, 0, v89
	v_cvt_pk_bf16_f32 v86, v86, v87
	v_cvt_pk_bf16_f32 v87, v88, v89
	ds_write_b64 v107, v[86:87] offset:16384
	v_max_f32_e32 v84, 0, v84
	v_max_f32_e32 v85, 0, v85
	v_cvt_pk_bf16_f32 v82, v82, v83
	v_cvt_pk_bf16_f32 v83, v84, v85
	ds_write_b64 v92, v[82:83] offset:24576
	v_max_f32_e32 v80, 0, v80
	v_max_f32_e32 v81, 0, v81
	v_cvt_pk_bf16_f32 v78, v78, v79
	v_cvt_pk_bf16_f32 v79, v80, v81
	ds_write_b64 v107, v[78:79] offset:32768
	v_max_f32_e32 v76, 0, v76
	v_max_f32_e32 v77, 0, v77
	v_cvt_pk_bf16_f32 v74, v74, v75
	v_cvt_pk_bf16_f32 v75, v76, v77
	ds_write_b64 v92, v[74:75] offset:40960
	v_max_f32_e32 v72, 0, v72
	v_max_f32_e32 v73, 0, v73
	v_cvt_pk_bf16_f32 v70, v70, v71
	v_cvt_pk_bf16_f32 v71, v72, v73
	ds_write_b64 v107, v[70:71] offset:49152
	v_max_f32_e32 v68, 0, v68
	v_max_f32_e32 v69, 0, v69
	v_cvt_pk_bf16_f32 v67, v68, v69
	ds_write_b64 v92, v[66:67] offset:57344
	v_or_b32_e32 v66, 32, v104
	v_lshrrev_b32_e32 v70, 3, v66
	global_load_dwordx4 v[66:69], v105, s[6:7] offset:192
	s_waitcnt vmcnt(1)
	v_add_f32_e32 v62, v62, v94
	v_add_f32_e32 v63, v63, v95
	v_add_f32_e32 v64, v64, v96
	v_add_f32_e32 v58, v58, v94
	v_add_f32_e32 v59, v59, v95
	v_add_f32_e32 v60, v60, v96
	v_max_f32_e32 v62, 0, v62
	v_max_f32_e32 v63, 0, v63
	v_max_f32_e32 v64, 0, v64
	v_add_f32_e32 v65, v65, v97
	v_max_f32_e32 v58, 0, v58
	v_max_f32_e32 v59, 0, v59
	v_max_f32_e32 v60, 0, v60
	v_add_f32_e32 v61, v61, v97
	v_max_f32_e32 v65, 0, v65
	v_cvt_pk_bf16_f32 v62, v62, v63
	v_cvt_pk_bf16_f32 v63, v64, v65
	v_xor_b32_e32 v64, v70, v179
	v_max_f32_e32 v61, 0, v61
	v_cvt_pk_bf16_f32 v58, v58, v59
	v_cvt_pk_bf16_f32 v59, v60, v61
	v_bitop3_b32 v60, v70, v179, 16 bitop3:0x1e
	v_add_f32_e32 v34, v34, v94
	v_lshlrev_b32_e32 v64, 4, v64
	v_lshlrev_b32_e32 v60, 4, v60
	v_add_f32_e32 v54, v54, v94
	v_add_f32_e32 v55, v55, v95
	v_add_f32_e32 v50, v50, v94
	v_add_f32_e32 v51, v51, v95
	v_add_f32_e32 v46, v46, v94
	v_add_f32_e32 v47, v47, v95
	v_add_f32_e32 v42, v42, v94
	v_add_f32_e32 v43, v43, v95
	v_add_f32_e32 v38, v38, v94
	v_add_f32_e32 v39, v39, v95
	v_max_f32_e32 v34, 0, v34
	v_add_f32_e32 v35, v35, v95
	v_add3_u32 v64, v103, v64, v102
	v_add3_u32 v60, v103, v60, v102
	v_max_f32_e32 v54, 0, v54
	v_max_f32_e32 v55, 0, v55
	v_add_f32_e32 v56, v56, v96
	v_add_f32_e32 v57, v57, v97
	v_max_f32_e32 v50, 0, v50
	v_max_f32_e32 v51, 0, v51
	v_add_f32_e32 v52, v52, v96
	v_add_f32_e32 v53, v53, v97
	v_max_f32_e32 v46, 0, v46
	v_max_f32_e32 v47, 0, v47
	v_add_f32_e32 v48, v48, v96
	v_add_f32_e32 v49, v49, v97
	v_max_f32_e32 v42, 0, v42
	v_max_f32_e32 v43, 0, v43
	v_add_f32_e32 v44, v44, v96
	v_add_f32_e32 v45, v45, v97
	v_max_f32_e32 v38, 0, v38
	v_max_f32_e32 v39, 0, v39
	v_add_f32_e32 v40, v40, v96
	v_add_f32_e32 v41, v41, v97
	v_max_f32_e32 v35, 0, v35
	v_add_f32_e32 v36, v36, v96
	v_add_f32_e32 v37, v37, v97
	v_cvt_pk_bf16_f32 v34, v34, v35
	ds_write_b64 v64, v[62:63]
	ds_write_b64 v60, v[58:59] offset:8192
	v_max_f32_e32 v56, 0, v56
	v_max_f32_e32 v57, 0, v57
	v_cvt_pk_bf16_f32 v54, v54, v55
	v_cvt_pk_bf16_f32 v55, v56, v57
	ds_write_b64 v64, v[54:55] offset:16384
	v_max_f32_e32 v52, 0, v52
	v_max_f32_e32 v53, 0, v53
	v_cvt_pk_bf16_f32 v50, v50, v51
	v_cvt_pk_bf16_f32 v51, v52, v53
	ds_write_b64 v60, v[50:51] offset:24576
	v_max_f32_e32 v48, 0, v48
	v_max_f32_e32 v49, 0, v49
	v_cvt_pk_bf16_f32 v46, v46, v47
	v_cvt_pk_bf16_f32 v47, v48, v49
	ds_write_b64 v64, v[46:47] offset:32768
	v_max_f32_e32 v44, 0, v44
	v_max_f32_e32 v45, 0, v45
	v_cvt_pk_bf16_f32 v42, v42, v43
	v_cvt_pk_bf16_f32 v43, v44, v45
	ds_write_b64 v60, v[42:43] offset:40960
	v_max_f32_e32 v40, 0, v40
	v_max_f32_e32 v41, 0, v41
	v_cvt_pk_bf16_f32 v38, v38, v39
	v_cvt_pk_bf16_f32 v39, v40, v41
	ds_write_b64 v64, v[38:39] offset:49152
	v_max_f32_e32 v36, 0, v36
	v_max_f32_e32 v37, 0, v37
	v_cvt_pk_bf16_f32 v35, v36, v37
	ds_write_b64 v60, v[34:35] offset:57344
	v_or_b32_e32 v34, 48, v104
	s_waitcnt vmcnt(0)
	v_add_f32_e32 v30, v30, v66
	v_add_f32_e32 v31, v31, v67
	v_add_f32_e32 v32, v32, v68
	v_add_f32_e32 v26, v26, v66
	v_add_f32_e32 v27, v27, v67
	v_add_f32_e32 v28, v28, v68
	v_lshrrev_b32_e32 v34, 3, v34
	v_max_f32_e32 v30, 0, v30
	v_max_f32_e32 v31, 0, v31
	v_max_f32_e32 v32, 0, v32
	v_add_f32_e32 v33, v33, v69
	v_max_f32_e32 v26, 0, v26
	v_max_f32_e32 v27, 0, v27
	v_max_f32_e32 v28, 0, v28
	v_add_f32_e32 v29, v29, v69
	v_max_f32_e32 v33, 0, v33
	v_cvt_pk_bf16_f32 v30, v30, v31
	v_cvt_pk_bf16_f32 v31, v32, v33
	v_xor_b32_e32 v32, v34, v179
	v_max_f32_e32 v29, 0, v29
	v_cvt_pk_bf16_f32 v26, v26, v27
	v_cvt_pk_bf16_f32 v27, v28, v29
	v_bitop3_b32 v28, v34, v179, 16 bitop3:0x1e
	v_add_f32_e32 v2, v2, v66
	v_lshlrev_b32_e32 v32, 4, v32
	v_lshlrev_b32_e32 v28, 4, v28
	v_add_f32_e32 v22, v22, v66
	v_add_f32_e32 v23, v23, v67
	v_add_f32_e32 v18, v18, v66
	v_add_f32_e32 v19, v19, v67
	v_add_f32_e32 v14, v14, v66
	v_add_f32_e32 v15, v15, v67
	v_add_f32_e32 v10, v10, v66
	v_add_f32_e32 v11, v11, v67
	v_add_f32_e32 v6, v6, v66
	v_add_f32_e32 v7, v7, v67
	v_max_f32_e32 v2, 0, v2
	v_add_f32_e32 v3, v3, v67
	v_add3_u32 v32, v103, v32, v102
	v_add3_u32 v28, v103, v28, v102
	v_max_f32_e32 v22, 0, v22
	v_max_f32_e32 v23, 0, v23
	v_add_f32_e32 v24, v24, v68
	v_add_f32_e32 v25, v25, v69
	v_max_f32_e32 v18, 0, v18
	v_max_f32_e32 v19, 0, v19
	v_add_f32_e32 v20, v20, v68
	v_add_f32_e32 v21, v21, v69
	v_max_f32_e32 v14, 0, v14
	v_max_f32_e32 v15, 0, v15
	v_add_f32_e32 v16, v16, v68
	v_add_f32_e32 v17, v17, v69
	v_max_f32_e32 v10, 0, v10
	v_max_f32_e32 v11, 0, v11
	v_add_f32_e32 v12, v12, v68
	v_add_f32_e32 v13, v13, v69
	v_max_f32_e32 v6, 0, v6
	v_max_f32_e32 v7, 0, v7
	v_add_f32_e32 v8, v8, v68
	v_add_f32_e32 v9, v9, v69
	v_max_f32_e32 v3, 0, v3
	v_add_f32_e32 v4, v4, v68
	v_add_f32_e32 v5, v5, v69
	v_cvt_pk_bf16_f32 v2, v2, v3
	ds_write_b64 v32, v[30:31]
	ds_write_b64 v28, v[26:27] offset:8192
	v_max_f32_e32 v24, 0, v24
	v_max_f32_e32 v25, 0, v25
	v_cvt_pk_bf16_f32 v22, v22, v23
	v_cvt_pk_bf16_f32 v23, v24, v25
	ds_write_b64 v32, v[22:23] offset:16384
	v_max_f32_e32 v20, 0, v20
	v_max_f32_e32 v21, 0, v21
	v_cvt_pk_bf16_f32 v18, v18, v19
	v_cvt_pk_bf16_f32 v19, v20, v21
	ds_write_b64 v28, v[18:19] offset:24576
	v_max_f32_e32 v16, 0, v16
	v_max_f32_e32 v17, 0, v17
	v_cvt_pk_bf16_f32 v14, v14, v15
	v_cvt_pk_bf16_f32 v15, v16, v17
	ds_write_b64 v32, v[14:15] offset:32768
	v_max_f32_e32 v12, 0, v12
	v_max_f32_e32 v13, 0, v13
	v_cvt_pk_bf16_f32 v10, v10, v11
	v_cvt_pk_bf16_f32 v11, v12, v13
	ds_write_b64 v28, v[10:11] offset:40960
	v_max_f32_e32 v8, 0, v8
	v_max_f32_e32 v9, 0, v9
	v_cvt_pk_bf16_f32 v6, v6, v7
	v_cvt_pk_bf16_f32 v7, v8, v9
	ds_write_b64 v32, v[6:7] offset:49152
	v_max_f32_e32 v4, 0, v4
	v_max_f32_e32 v5, 0, v5
	v_cvt_pk_bf16_f32 v3, v4, v5
	ds_write_b64 v28, v[2:3] offset:57344
	v_and_b32_e32 v2, 0x1f0, v1
	v_lshrrev_b32_e32 v1, 5, v0
	v_xor_b32_e32 v4, v1, v0
	v_mov_b32_e32 v3, 0
	v_lshlrev_b32_e32 v4, 4, v4
	v_lshl_add_u64 v[12:13], s[4:5], 0, v[2:3]
	v_lshlrev_b32_e32 v2, 9, v1
	v_and_b32_e32 v16, 0x1f0, v4
	v_add3_u32 v2, 0, v2, v16
	s_waitcnt lgkmcnt(0)
	s_barrier
	ds_read_b128 v[4:7], v2
	v_lshlrev_b32_e32 v2, 11, v1
	v_lshl_add_u64 v[14:15], v[12:13], 0, v[2:3]
	v_or_b32_e32 v2, 0x200, v0
	v_lshrrev_b32_e32 v2, 5, v2
	v_xor_b32_e32 v9, v2, v0
	v_lshlrev_b32_e32 v9, 4, v9
	v_lshlrev_b32_e32 v8, 9, v2
	v_and_b32_e32 v9, 0x1f0, v9
	v_add3_u32 v8, 0, v8, v9
	ds_read_b128 v[8:11], v8
	v_lshlrev_b32_e32 v2, 11, v2
	s_waitcnt lgkmcnt(1)
	global_store_dwordx4 v[14:15], v[4:7], off sc1
	s_nop 1
	v_lshl_add_u64 v[4:5], v[12:13], 0, v[2:3]
	s_waitcnt lgkmcnt(0)
	global_store_dwordx4 v[4:5], v[8:11], off sc1
	v_or_b32_e32 v2, 32, v1
	v_lshlrev_b32_e32 v4, 9, v2
	v_or_b32_e32 v8, 0x600, v0
	v_lshrrev_b32_e32 v17, 5, v8
	v_xor_b32_e32 v9, v17, v0
	v_lshlrev_b32_e32 v9, 4, v9
	v_add3_u32 v4, 0, v4, v16
	v_lshlrev_b32_e32 v8, 9, v17
	v_and_b32_e32 v9, 0x1f0, v9
	ds_read_b128 v[4:7], v4
	v_add3_u32 v8, 0, v8, v9
	ds_read_b128 v[8:11], v8
	v_lshlrev_b32_e32 v2, 11, v2
	v_lshl_add_u64 v[14:15], v[12:13], 0, v[2:3]
	v_lshlrev_b32_e32 v2, 11, v17
	s_waitcnt lgkmcnt(1)
	global_store_dwordx4 v[14:15], v[4:7], off sc1
	s_nop 1
	v_lshl_add_u64 v[4:5], v[12:13], 0, v[2:3]
	s_waitcnt lgkmcnt(0)
	global_store_dwordx4 v[4:5], v[8:11], off sc1
	v_or_b32_e32 v2, 64, v1
	v_lshlrev_b32_e32 v4, 9, v2
	v_or_b32_e32 v8, 0xa00, v0
	v_lshrrev_b32_e32 v17, 5, v8
	v_xor_b32_e32 v9, v17, v0
	v_lshlrev_b32_e32 v9, 4, v9
	v_add3_u32 v4, 0, v4, v16
	v_lshlrev_b32_e32 v8, 9, v17
	v_and_b32_e32 v9, 0x1f0, v9
	ds_read_b128 v[4:7], v4
	v_add3_u32 v8, 0, v8, v9
	ds_read_b128 v[8:11], v8
	v_lshlrev_b32_e32 v2, 11, v2
	v_lshl_add_u64 v[14:15], v[12:13], 0, v[2:3]
	v_lshlrev_b32_e32 v2, 11, v17
	s_waitcnt lgkmcnt(1)
	global_store_dwordx4 v[14:15], v[4:7], off sc1
	s_nop 1
	v_lshl_add_u64 v[4:5], v[12:13], 0, v[2:3]
	s_waitcnt lgkmcnt(0)
	global_store_dwordx4 v[4:5], v[8:11], off sc1
	v_or_b32_e32 v2, 0x60, v1
	v_lshlrev_b32_e32 v4, 9, v2
	v_or_b32_e32 v8, 0xe00, v0
	v_lshrrev_b32_e32 v17, 5, v8
	v_xor_b32_e32 v9, v17, v0
	v_lshlrev_b32_e32 v9, 4, v9
	v_add3_u32 v4, 0, v4, v16
	v_lshlrev_b32_e32 v8, 9, v17
	v_and_b32_e32 v9, 0x1f0, v9
	ds_read_b128 v[4:7], v4
	v_add3_u32 v8, 0, v8, v9
	ds_read_b128 v[8:11], v8
	v_lshlrev_b32_e32 v2, 11, v2
	v_lshl_add_u64 v[14:15], v[12:13], 0, v[2:3]
	v_lshlrev_b32_e32 v2, 11, v17
	s_waitcnt lgkmcnt(1)
	global_store_dwordx4 v[14:15], v[4:7], off sc1
	s_nop 1
	v_lshl_add_u64 v[4:5], v[12:13], 0, v[2:3]
	s_waitcnt lgkmcnt(0)
	global_store_dwordx4 v[4:5], v[8:11], off sc1
	v_or_b32_e32 v2, 0x80, v1
	v_lshlrev_b32_e32 v4, 9, v2
	v_or_b32_e32 v8, 0x1200, v0
	v_lshrrev_b32_e32 v17, 5, v8
	v_xor_b32_e32 v9, v17, v0
	v_lshlrev_b32_e32 v9, 4, v9
	v_add3_u32 v4, 0, v4, v16
	v_lshlrev_b32_e32 v8, 9, v17
	v_and_b32_e32 v9, 0x1f0, v9
	ds_read_b128 v[4:7], v4
	v_add3_u32 v8, 0, v8, v9
	ds_read_b128 v[8:11], v8
	v_lshlrev_b32_e32 v2, 11, v2
	v_lshl_add_u64 v[14:15], v[12:13], 0, v[2:3]
	v_lshlrev_b32_e32 v2, 11, v17
	s_waitcnt lgkmcnt(1)
	global_store_dwordx4 v[14:15], v[4:7], off sc1
	s_nop 1
	v_lshl_add_u64 v[4:5], v[12:13], 0, v[2:3]
	s_waitcnt lgkmcnt(0)
	global_store_dwordx4 v[4:5], v[8:11], off sc1
	v_or_b32_e32 v2, 0xa0, v1
	v_lshlrev_b32_e32 v4, 9, v2
	v_or_b32_e32 v8, 0x1600, v0
	v_lshrrev_b32_e32 v17, 5, v8
	v_xor_b32_e32 v9, v17, v0
	v_lshlrev_b32_e32 v9, 4, v9
	v_add3_u32 v4, 0, v4, v16
	v_lshlrev_b32_e32 v8, 9, v17
	v_and_b32_e32 v9, 0x1f0, v9
	ds_read_b128 v[4:7], v4
	v_add3_u32 v8, 0, v8, v9
	ds_read_b128 v[8:11], v8
	v_lshlrev_b32_e32 v2, 11, v2
	v_lshl_add_u64 v[14:15], v[12:13], 0, v[2:3]
	v_lshlrev_b32_e32 v2, 11, v17
	s_waitcnt lgkmcnt(1)
	global_store_dwordx4 v[14:15], v[4:7], off sc1
	s_nop 1
	v_lshl_add_u64 v[4:5], v[12:13], 0, v[2:3]
	s_waitcnt lgkmcnt(0)
	global_store_dwordx4 v[4:5], v[8:11], off sc1
	v_or_b32_e32 v2, 0xc0, v1
	v_lshlrev_b32_e32 v4, 9, v2
	v_or_b32_e32 v8, 0x1a00, v0
	v_lshrrev_b32_e32 v17, 5, v8
	v_xor_b32_e32 v9, v17, v0
	v_add3_u32 v4, 0, v4, v16
	v_lshlrev_b32_e32 v9, 4, v9
	ds_read_b128 v[4:7], v4
	v_lshlrev_b32_e32 v8, 9, v17
	v_and_b32_e32 v9, 0x1f0, v9
	v_add3_u32 v8, 0, v8, v9
	ds_read_b128 v[8:11], v8
	v_lshlrev_b32_e32 v2, 11, v2
	v_lshl_add_u64 v[14:15], v[12:13], 0, v[2:3]
	v_lshlrev_b32_e32 v2, 11, v17
	v_or_b32_e32 v1, 0xe0, v1
	s_waitcnt lgkmcnt(1)
	global_store_dwordx4 v[14:15], v[4:7], off sc1
	s_nop 1
	v_lshl_add_u64 v[4:5], v[12:13], 0, v[2:3]
	v_lshlrev_b32_e32 v2, 9, v1
	v_add3_u32 v2, 0, v2, v16
	s_waitcnt lgkmcnt(0)
	global_store_dwordx4 v[4:5], v[8:11], off sc1
	ds_read_b128 v[4:7], v2
	v_lshlrev_b32_e32 v2, 11, v1
	v_or_b32_e32 v1, 0x1e00, v0
	v_lshrrev_b32_e32 v1, 5, v1
	v_xor_b32_e32 v9, v1, v0
	v_lshlrev_b32_e32 v9, 4, v9
	v_lshlrev_b32_e32 v8, 9, v1
	v_and_b32_e32 v9, 0x1f0, v9
	v_add3_u32 v8, 0, v8, v9
	ds_read_b128 v[8:11], v8
	v_lshl_add_u64 v[14:15], v[12:13], 0, v[2:3]
	v_lshlrev_b32_e32 v2, 11, v1
	s_waitcnt lgkmcnt(1)
	global_store_dwordx4 v[14:15], v[4:7], off sc1
	s_nop 1
	v_lshl_add_u64 v[4:5], v[12:13], 0, v[2:3]
	s_waitcnt lgkmcnt(0)
	global_store_dwordx4 v[4:5], v[8:11], off sc1
	s_waitcnt lgkmcnt(0)
	s_barrier
	s_lshl_b32 s3, s2, 3
	s_and_b32 s3, s3, 56
	s_ashr_i32 s17, s2, 5
	s_add_i32 s20, s3, s17
	s_ashr_i32 s21, s20, 31
	s_bfe_u32 s16, s2, 0x20003
	s_lshl_b64 s[4:5], s[20:21], 17
	s_lshl_b64 s[6:7], s[20:21], 19
	s_add_u32 s6, s12, s6
	s_addc_u32 s7, s13, s7
	s_lshl_b32 s3, s16, 19
	s_add_u32 s3, s14, s3
	v_ashrrev_i32_e32 v2, 6, v0
	v_lshlrev_b32_e32 v1, 4, v0
	s_addc_u32 s13, s15, 0
	v_lshlrev_b32_e32 v4, 9, v2
	v_and_b32_e32 v5, 0x1f0, v1
	s_add_u32 s12, s3, 0x400000
	v_and_or_b32 v32, v4, s0, v5
	v_lshlrev_b32_e32 v4, 5, v2
	v_and_b32_e32 v5, 48, v1
	s_addc_u32 s13, s13, 0
	v_bitop3_b32 v4, v4, v5, 32 bitop3:0x6c
	s_and_b32 s15, s2, 8
	s_add_i32 s3, s20, 3
	v_bfe_u32 v31, v0, 5, 1
	v_lshrrev_b32_e32 v34, 1, v4
	v_add_u32_e32 v4, s15, v2
	s_mov_b32 s20, 0x3ffffe
	v_and_or_b32 v30, v4, s20, v31
	v_bfe_i32 v5, v30, 0, 22
	v_bfe_u32 v4, v30, 21, 1
	v_add_u32_e32 v6, v5, v4
	v_lshlrev_b32_e32 v4, 3, v6
	v_and_b32_e32 v6, 0x7fffffe, v6
	s_lshl_b32 s0, s17, 4
	v_sub_u32_e32 v5, v5, v6
	s_and_b32 s17, s0, 16
	v_lshl_or_b32 v6, v5, 5, v34
	v_add_u32_e32 v5, s17, v2
	v_and_or_b32 v35, v5, s20, v31
	v_bfe_i32 v7, v35, 0, 22
	v_bfe_u32 v8, v35, 21, 1
	v_add_u32_e32 v8, v7, v8
	v_lshlrev_b32_e32 v9, 3, v8
	v_and_b32_e32 v8, 0x7fffffe, v8
	v_add_u32_e32 v5, 8, v5
	v_sub_u32_e32 v7, v7, v8
	v_and_or_b32 v36, v5, s20, v31
	v_lshl_or_b32 v98, v7, 5, v34
	v_bfe_i32 v5, v36, 0, 22
	v_bfe_u32 v7, v36, 21, 1
	v_add_u32_e32 v7, v5, v7
	v_lshrrev_b32_e32 v33, 6, v32
	v_lshlrev_b32_e32 v8, 3, v7
	v_and_b32_e32 v7, 0x7fffffe, v7
	s_and_b32 s3, s3, 15
	v_and_or_b32 v4, v4, -16, v33
	v_sub_u32_e32 v5, v5, v7
	v_and_or_b32 v14, v9, -16, v33
	v_lshl_or_b32 v100, v5, 5, v34
	v_ashrrev_i32_e32 v5, 31, v4
	s_lshl_b32 s14, s3, 6
	s_lshl_b32 s0, s3, 8
	s_lshl_b32 s2, s3, 7
	v_and_or_b32 v16, v8, -16, v33
	v_lshlrev_b64 v[4:5], 12, v[4:5]
	s_add_u32 s2, s12, s2
	v_ashrrev_i32_e32 v15, 31, v14
	v_lshl_add_u64 v[4:5], s[6:7], 0, v[4:5]
	v_ashrrev_i32_e32 v7, 31, v6
	s_addc_u32 s3, s13, 0
	v_lshlrev_b64 v[102:103], 11, v[14:15]
	v_ashrrev_i32_e32 v99, 31, v98
	v_ashrrev_i32_e32 v17, 31, v16
	v_lshl_add_u64 v[8:9], v[4:5], 0, s[0:1]
	v_lshlrev_b64 v[38:39], 2, v[6:7]
	v_lshl_add_u64 v[14:15], s[2:3], 0, v[102:103]
	v_lshlrev_b64 v[22:23], 1, v[98:99]
	v_lshlrev_b64 v[104:105], 11, v[16:17]
	v_ashrrev_i32_e32 v101, 31, v100
	v_lshl_add_u64 v[18:19], v[8:9], 0, v[38:39]
	v_lshl_add_u64 v[24:25], v[14:15], 0, v[22:23]
	v_lshl_add_u64 v[14:15], s[2:3], 0, v[104:105]
	v_lshlrev_b64 v[26:27], 1, v[100:101]
	global_load_dwordx4 v[6:9], v[18:19], off offset:16
	global_load_dwordx4 v[10:13], v[18:19], off
	v_lshl_add_u64 v[28:29], v[14:15], 0, v[26:27]
	global_load_dwordx4 v[14:17], v[24:25], off
	global_load_dwordx4 v[18:21], v[28:29], off
	v_lshlrev_b32_e32 v24, 10, v30
	v_or_b32_e32 v125, v24, v32
	v_xad_u32 v24, s15, 8, v2
	v_and_or_b32 v24, v24, s20, v31
	v_lshlrev_b32_e32 v25, 10, v24
	v_or_b32_e32 v122, v25, v32
	v_bfe_i32 v25, v24, 0, 22
	v_bfe_u32 v24, v24, 21, 1
	v_add_u32_e32 v28, v25, v24
	v_lshlrev_b32_e32 v24, 3, v28
	v_and_b32_e32 v28, 0x7fffffe, v28
	v_sub_u32_e32 v25, v25, v28
	v_lshl_or_b32 v28, v25, 5, v34
	v_lshlrev_b32_e32 v25, 10, v35
	v_or_b32_e32 v126, v25, v32
	v_lshlrev_b32_e32 v25, 10, v36
	v_or_b32_e32 v127, v25, v32
	v_xad_u32 v25, s17, 16, v2
	v_and_or_b32 v25, v25, s20, v31
	v_lshlrev_b32_e32 v29, 10, v25
	v_or_b32_e32 v123, v29, v32
	v_bfe_i32 v29, v25, 0, 22
	v_bfe_u32 v25, v25, 21, 1
	v_add_u32_e32 v25, v29, v25
	v_and_b32_e32 v121, 3, v2
	v_lshlrev_b32_e32 v30, 3, v25
	v_and_b32_e32 v25, 0x7fffffe, v25
	v_xad_u32 v2, s17, 24, v2
	v_sub_u32_e32 v25, v29, v25
	v_and_or_b32 v2, v2, s20, v31
	v_lshl_or_b32 v106, v25, 5, v34
	v_lshlrev_b32_e32 v25, 10, v2
	v_or_b32_e32 v124, v25, v32
	v_bfe_i32 v25, v2, 0, 22
	v_bfe_u32 v2, v2, 21, 1
	v_add_u32_e32 v2, v25, v2
	v_lshlrev_b32_e32 v29, 3, v2
	v_and_b32_e32 v2, 0x7fffffe, v2
	v_and_b32_e32 v118, 15, v0
	v_sub_u32_e32 v2, v25, v2
	v_lshlrev_b32_e32 v25, 2, v0
	v_ashrrev_i32_e32 v120, 8, v0
	v_and_or_b32 v32, v29, -16, v33
	v_lshl_or_b32 v108, v2, 5, v34
	v_and_b32_e32 v2, 48, v0
	v_and_b32_e32 v25, 32, v25
	v_lshlrev_b32_e32 v29, 6, v118
	v_and_b32_e32 v119, 63, v0
	v_and_or_b32 v24, v24, -16, v33
	v_and_or_b32 v30, v30, -16, v33
	v_lshlrev_b32_e32 v68, 13, v120
	v_bitop3_b32 v2, v29, v25, v2 bitop3:0x36
	v_ashrrev_i32_e32 v25, 31, v24
	v_lshlrev_b64 v[24:25], 12, v[24:25]
	v_lshl_add_u64 v[56:57], s[6:7], 0, v[24:25]
	v_ashrrev_i32_e32 v29, 31, v28
	v_lshl_add_u64 v[24:25], v[56:57], 0, s[0:1]
	v_lshlrev_b64 v[58:59], 2, v[28:29]
	v_ashrrev_i32_e32 v31, 31, v30
	v_lshl_add_u64 v[24:25], v[24:25], 0, v[58:59]
	v_lshlrev_b64 v[110:111], 11, v[30:31]
	v_ashrrev_i32_e32 v107, 31, v106
	v_ashrrev_i32_e32 v33, 31, v32
	global_load_dwordx4 v[40:43], v[24:25], off offset:16
	global_load_dwordx4 v[44:47], v[24:25], off
	v_lshl_add_u64 v[24:25], s[2:3], 0, v[110:111]
	v_lshlrev_b64 v[60:61], 1, v[106:107]
	v_lshlrev_b64 v[112:113], 11, v[32:33]
	v_ashrrev_i32_e32 v109, 31, v108
	v_lshl_add_u64 v[24:25], v[24:25], 0, v[60:61]
	v_lshl_add_u64 v[28:29], s[2:3], 0, v[112:113]
	v_lshlrev_b64 v[62:63], 1, v[108:109]
	v_lshl_add_u64 v[28:29], v[28:29], 0, v[62:63]
	global_load_dwordx4 v[48:51], v[24:25], off
	global_load_dwordx4 v[52:55], v[28:29], off
	s_add_i32 s0, s14, 64
	s_and_b32 s2, s0, 0x3c0
	s_lshl_b32 s0, s2, 2
	s_lshl_b32 s2, s2, 1
	v_lshl_add_u64 v[24:25], v[4:5], 0, s[0:1]
	s_add_u32 s2, s12, s2
	v_lshl_add_u64 v[24:25], v[24:25], 0, v[38:39]
	s_addc_u32 s3, s13, 0
	global_load_dwordx4 v[30:33], v[24:25], off offset:16
	global_load_dwordx4 v[34:37], v[24:25], off
	v_lshl_add_u64 v[24:25], s[2:3], 0, v[102:103]
	v_lshl_add_u64 v[64:65], v[24:25], 0, v[22:23]
	v_lshl_add_u64 v[22:23], s[2:3], 0, v[104:105]
	v_lshl_add_u64 v[66:67], v[22:23], 0, v[26:27]
	global_load_dwordx4 v[26:29], v[64:65], off
	global_load_dwordx4 v[22:25], v[66:67], off
	v_add_u32_e32 v64, 0, v125
	s_waitcnt vmcnt(10)
	v_cvt_pk_bf16_f32 v10, v10, v11
	v_cvt_pk_bf16_f32 v11, v12, v13
	v_cvt_pk_bf16_f32 v12, v6, v7
	v_add_u32_e32 v6, 0, v126
	v_cvt_pk_bf16_f32 v13, v8, v9
	ds_write_b128 v64, v[10:13]
	s_waitcnt vmcnt(9)
	ds_write_b128 v6, v[14:17] offset:32768
	v_add_u32_e32 v6, 0, v127
	s_waitcnt vmcnt(8)
	ds_write_b128 v6, v[18:21] offset:32768
	v_add_u32_e32 v10, 0, v122
	s_waitcnt vmcnt(6)
	v_cvt_pk_bf16_f32 v6, v44, v45
	v_cvt_pk_bf16_f32 v7, v46, v47
	v_cvt_pk_bf16_f32 v8, v40, v41
	v_cvt_pk_bf16_f32 v9, v42, v43
	ds_write_b128 v10, v[6:9]
	v_add_u32_e32 v6, 0, v123
	s_waitcnt vmcnt(5)
	ds_write_b128 v6, v[48:51] offset:32768
	v_add_u32_e32 v6, 0, v124
	s_waitcnt vmcnt(4)
	ds_write_b128 v6, v[52:55] offset:32768
	v_lshl_add_u64 v[6:7], v[56:57], 0, s[0:1]
	v_lshl_add_u64 v[14:15], v[6:7], 0, v[58:59]
	global_load_dwordx4 v[6:9], v[14:15], off offset:16
	global_load_dwordx4 v[10:13], v[14:15], off
	v_lshl_add_u64 v[14:15], s[2:3], 0, v[110:111]
	v_lshl_add_u64 v[40:41], v[14:15], 0, v[60:61]
	v_lshl_add_u64 v[14:15], s[2:3], 0, v[112:113]
	v_lshl_add_u64 v[42:43], v[14:15], 0, v[62:63]
	global_load_dwordx4 v[18:21], v[40:41], off
	global_load_dwordx4 v[14:17], v[42:43], off
	v_lshlrev_b32_e32 v40, 13, v121
	s_cmp_lg_u32 0, -1
	s_waitcnt lgkmcnt(0)
	s_cselect_b32 s0, 0, 0
	v_add3_u32 v128, v68, s0, v2
	s_add_i32 s0, s0, 0x8000
	v_add3_u32 v129, v40, s0, v2
	v_lshl_add_u64 v[114:115], v[4:5], 0, v[38:39]
	v_lshl_add_u64 v[116:117], v[56:57], 0, v[58:59]
	s_add_i32 s2, s14, 0x80
	s_mov_b32 s3, 0
	v_mov_b32_e32 v2, v3
	v_mov_b32_e32 v4, v3
	v_mov_b32_e32 v5, v3
	v_mov_b32_e32 v38, v3
	v_mov_b32_e32 v39, v3
	v_mov_b32_e32 v40, v3
	v_mov_b32_e32 v41, v3
	v_mov_b32_e32 v42, v3
	v_mov_b32_e32 v43, v3
	v_mov_b32_e32 v44, v3
	v_mov_b32_e32 v45, v3
	v_mov_b32_e32 v46, v3
	v_mov_b32_e32 v47, v3
	v_mov_b32_e32 v48, v3
	v_mov_b32_e32 v49, v3
	v_mov_b32_e32 v50, v3
	v_mov_b32_e32 v51, v3
	v_mov_b32_e32 v52, v3
	v_mov_b32_e32 v53, v3
	v_mov_b32_e32 v54, v3
	v_mov_b32_e32 v55, v3
	v_mov_b32_e32 v56, v3
	v_mov_b32_e32 v57, v3
	v_mov_b32_e32 v58, v3
	v_mov_b32_e32 v59, v3
	v_mov_b32_e32 v60, v3
	v_mov_b32_e32 v61, v3
	v_mov_b32_e32 v62, v3
	v_mov_b32_e32 v63, v3
	v_mov_b32_e32 v64, v3
	v_mov_b32_e32 v65, v3
	v_mov_b32_e32 v66, v3
	v_mov_b32_e32 v67, v3
	v_mov_b32_e32 v68, v3
	v_mov_b32_e32 v69, v3
	v_mov_b32_e32 v70, v3
	v_mov_b32_e32 v71, v3
	v_mov_b32_e32 v72, v3
	v_mov_b32_e32 v73, v3
	v_mov_b32_e32 v74, v3
	v_mov_b32_e32 v75, v3
	v_mov_b32_e32 v76, v3
	v_mov_b32_e32 v77, v3
	v_mov_b32_e32 v78, v3
	v_mov_b32_e32 v79, v3
	v_mov_b32_e32 v80, v3
	v_mov_b32_e32 v81, v3
	v_mov_b32_e32 v82, v3
	v_mov_b32_e32 v83, v3
	v_mov_b32_e32 v84, v3
	v_mov_b32_e32 v85, v3
	v_mov_b32_e32 v86, v3
	v_mov_b32_e32 v87, v3
	v_mov_b32_e32 v88, v3
	v_mov_b32_e32 v89, v3
	v_mov_b32_e32 v90, v3
	v_mov_b32_e32 v91, v3
	v_mov_b32_e32 v92, v3
	v_mov_b32_e32 v93, v3
	v_mov_b32_e32 v94, v3
	v_mov_b32_e32 v95, v3
	v_mov_b32_e32 v96, v3
	v_mov_b32_e32 v97, v3
	s_and_b32 s0, s3, 0x10000
	v_add_u32_e32 v158, s0, v128
	v_add_u32_e32 v159, s0, v129
	s_barrier
.LBB1_3:
	ds_read_b128 v[130:133], v159 offset:0
	ds_read_b128 v[134:137], v159 offset:0x800
	ds_read_b128 v[138:141], v159 offset:0x1000
	ds_read_b128 v[142:145], v159 offset:0x1800
	ds_read_b128 v[146:149], v158 offset:0
	ds_read_b128 v[150:153], v158 offset:0x800
	ds_read_b128 v[154:157], v158 offset:0x1000
	s_waitcnt lgkmcnt(2)
	v_mfma_f32_16x16x32_bf16 v[94:97], v[130:133], v[146:149], v[94:97]
	v_mfma_f32_16x16x32_bf16 v[90:93], v[134:137], v[146:149], v[90:93]
	v_mfma_f32_16x16x32_bf16 v[86:89], v[138:141], v[146:149], v[86:89]
	v_mfma_f32_16x16x32_bf16 v[82:85], v[142:145], v[146:149], v[82:85]
	ds_read_b128 v[146:149], v158 offset:0x1800
	s_waitcnt lgkmcnt(2)
	v_mfma_f32_16x16x32_bf16 v[78:81], v[130:133], v[150:153], v[78:81]
	v_mfma_f32_16x16x32_bf16 v[74:77], v[134:137], v[150:153], v[74:77]
	v_mfma_f32_16x16x32_bf16 v[70:73], v[138:141], v[150:153], v[70:73]
	v_mfma_f32_16x16x32_bf16 v[66:69], v[142:145], v[150:153], v[66:69]
	s_waitcnt lgkmcnt(1)
	v_mfma_f32_16x16x32_bf16 v[62:65], v[130:133], v[154:157], v[62:65]
	v_mfma_f32_16x16x32_bf16 v[58:61], v[134:137], v[154:157], v[58:61]
	v_mfma_f32_16x16x32_bf16 v[54:57], v[138:141], v[154:157], v[54:57]
	v_mfma_f32_16x16x32_bf16 v[50:53], v[142:145], v[154:157], v[50:53]
	s_waitcnt lgkmcnt(0)
	v_mfma_f32_16x16x32_bf16 v[46:49], v[130:133], v[146:149], v[46:49]
	v_mfma_f32_16x16x32_bf16 v[42:45], v[134:137], v[146:149], v[42:45]
	v_mfma_f32_16x16x32_bf16 v[38:41], v[138:141], v[146:149], v[38:41]
	v_mfma_f32_16x16x32_bf16 v[2:5], v[142:145], v[146:149], v[2:5]
	s_xor_b32 s0, s0, 0x10000
	s_and_b32 s6, s2, 0x3c0
	s_add_i32 s14, s0, 0
	s_lshl_b32 s0, s6, 2
	s_lshl_b32 s6, s6, 1
	s_add_u32 s6, s12, s6
	s_waitcnt vmcnt(6)
	v_cvt_pk_bf16_f32 v34, v34, v35
	v_cvt_pk_bf16_f32 v35, v36, v37
	v_cvt_pk_bf16_f32 v36, v30, v31
	v_cvt_pk_bf16_f32 v37, v32, v33
	v_add_u32_e32 v30, s14, v125
	s_addc_u32 s7, s13, 0
	v_add_u32_e32 v31, s14, v126
	v_add_u32_e32 v32, s14, v127
	ds_write_b128 v30, v[34:37]
	s_waitcnt vmcnt(5)
	ds_write_b128 v31, v[26:29] offset:32768
	s_waitcnt vmcnt(4)
	ds_write_b128 v32, v[22:25] offset:32768
	v_lshl_add_u64 v[22:23], s[6:7], 0, v[102:103]
	v_lshl_add_u64 v[24:25], s[6:7], 0, v[104:105]
	v_lshl_add_u64 v[130:131], v[114:115], 0, s[0:1]
	v_lshl_add_u64 v[22:23], v[98:99], 1, v[22:23]
	v_lshl_add_u64 v[24:25], v[100:101], 1, v[24:25]
	global_load_dwordx4 v[30:33], v[130:131], off offset:16
	global_load_dwordx4 v[34:37], v[130:131], off
	global_load_dwordx4 v[26:29], v[22:23], off
	s_nop 0
	global_load_dwordx4 v[22:25], v[24:25], off
	ds_read_b128 v[130:133], v159 offset:0x400
	ds_read_b128 v[134:137], v159 offset:0xc00
	ds_read_b128 v[138:141], v159 offset:0x1400
	ds_read_b128 v[142:145], v159 offset:0x1c00
	ds_read_b128 v[146:149], v158 offset:0x400
	ds_read_b128 v[150:153], v158 offset:0xc00
	ds_read_b128 v[154:157], v158 offset:0x1400
	s_waitcnt lgkmcnt(2)
	v_mfma_f32_16x16x32_bf16 v[94:97], v[130:133], v[146:149], v[94:97]
	v_mfma_f32_16x16x32_bf16 v[90:93], v[134:137], v[146:149], v[90:93]
	v_mfma_f32_16x16x32_bf16 v[86:89], v[138:141], v[146:149], v[86:89]
	v_mfma_f32_16x16x32_bf16 v[82:85], v[142:145], v[146:149], v[82:85]
	ds_read_b128 v[146:149], v158 offset:0x1c00
	s_waitcnt lgkmcnt(2)
	v_mfma_f32_16x16x32_bf16 v[78:81], v[130:133], v[150:153], v[78:81]
	v_mfma_f32_16x16x32_bf16 v[74:77], v[134:137], v[150:153], v[74:77]
	v_mfma_f32_16x16x32_bf16 v[70:73], v[138:141], v[150:153], v[70:73]
	v_mfma_f32_16x16x32_bf16 v[66:69], v[142:145], v[150:153], v[66:69]
	s_waitcnt lgkmcnt(1)
	v_mfma_f32_16x16x32_bf16 v[62:65], v[130:133], v[154:157], v[62:65]
	v_mfma_f32_16x16x32_bf16 v[58:61], v[134:137], v[154:157], v[58:61]
	v_mfma_f32_16x16x32_bf16 v[54:57], v[138:141], v[154:157], v[54:57]
	v_mfma_f32_16x16x32_bf16 v[50:53], v[142:145], v[154:157], v[50:53]
	s_waitcnt lgkmcnt(0)
	v_mfma_f32_16x16x32_bf16 v[46:49], v[130:133], v[146:149], v[46:49]
	v_mfma_f32_16x16x32_bf16 v[42:45], v[134:137], v[146:149], v[42:45]
	v_mfma_f32_16x16x32_bf16 v[38:41], v[138:141], v[146:149], v[38:41]
	v_mfma_f32_16x16x32_bf16 v[2:5], v[142:145], v[146:149], v[2:5]
	v_add_u32_e32 v130, s14, v122
	s_waitcnt vmcnt(6)
	v_cvt_pk_bf16_f32 v10, v10, v11
	v_cvt_pk_bf16_f32 v11, v12, v13
	v_cvt_pk_bf16_f32 v12, v6, v7
	v_add_u32_e32 v6, s14, v123
	v_cvt_pk_bf16_f32 v13, v8, v9
	ds_write_b128 v130, v[10:13]
	s_waitcnt vmcnt(5)
	ds_write_b128 v6, v[18:21] offset:32768
	v_add_u32_e32 v6, s14, v124
	s_waitcnt vmcnt(4)
	ds_write_b128 v6, v[14:17] offset:32768
	v_lshl_add_u64 v[14:15], s[6:7], 0, v[110:111]
	v_lshl_add_u64 v[16:17], s[6:7], 0, v[112:113]
	v_lshl_add_u64 v[10:11], v[116:117], 0, s[0:1]
	v_lshl_add_u64 v[14:15], v[106:107], 1, v[14:15]
	v_lshl_add_u64 v[16:17], v[108:109], 1, v[16:17]
	global_load_dwordx4 v[6:9], v[10:11], off offset:16
	s_nop 0
	global_load_dwordx4 v[10:13], v[10:11], off
	s_nop 0
	global_load_dwordx4 v[18:21], v[14:15], off
	s_nop 0
	global_load_dwordx4 v[14:17], v[16:17], off
	s_waitcnt lgkmcnt(0)
	s_add_i32 s2, s2, 64
	s_add_i32 s3, s3, 0x10000
	s_and_b32 s0, s3, 0x10000
	v_add_u32_e32 v158, s0, v128
	v_add_u32_e32 v159, s0, v129
	s_cmp_lg_u32 s3, 0xe0000
	s_barrier
	s_cbranch_scc1 .LBB1_3
	ds_read_b128 v[98:101], v129 offset:0
	ds_read_b128 v[102:105], v129 offset:0x800
	ds_read_b128 v[106:109], v129 offset:0x1000
	ds_read_b128 v[110:113], v129 offset:0x1800
	ds_read_b128 v[114:117], v128 offset:0
	ds_read_b128 v[130:133], v128 offset:0x800
	ds_read_b128 v[134:137], v128 offset:0x1000
	s_nop 0
	s_waitcnt lgkmcnt(2)
	s_nop 0
	v_mfma_f32_16x16x32_bf16 v[94:97], v[98:101], v[114:117], v[94:97]
	v_mfma_f32_16x16x32_bf16 v[90:93], v[102:105], v[114:117], v[90:93]
	v_mfma_f32_16x16x32_bf16 v[86:89], v[106:109], v[114:117], v[86:89]
	v_mfma_f32_16x16x32_bf16 v[82:85], v[110:113], v[114:117], v[82:85]
	ds_read_b128 v[114:117], v128 offset:0x1800
	s_waitcnt lgkmcnt(2)
	s_nop 0
	v_mfma_f32_16x16x32_bf16 v[78:81], v[98:101], v[130:133], v[78:81]
	v_mfma_f32_16x16x32_bf16 v[74:77], v[102:105], v[130:133], v[74:77]
	v_mfma_f32_16x16x32_bf16 v[70:73], v[106:109], v[130:133], v[70:73]
	v_mfma_f32_16x16x32_bf16 v[66:69], v[110:113], v[130:133], v[66:69]
	s_waitcnt lgkmcnt(1)
	s_nop 0
	v_mfma_f32_16x16x32_bf16 v[62:65], v[98:101], v[134:137], v[62:65]
	v_mfma_f32_16x16x32_bf16 v[58:61], v[102:105], v[134:137], v[58:61]
	v_mfma_f32_16x16x32_bf16 v[54:57], v[106:109], v[134:137], v[54:57]
	v_mfma_f32_16x16x32_bf16 v[50:53], v[110:113], v[134:137], v[50:53]
	s_waitcnt lgkmcnt(0)
	s_nop 0
	v_mfma_f32_16x16x32_bf16 v[46:49], v[98:101], v[114:117], v[46:49]
	v_mfma_f32_16x16x32_bf16 v[42:45], v[102:105], v[114:117], v[42:45]
	v_mfma_f32_16x16x32_bf16 v[38:41], v[106:109], v[114:117], v[38:41]
	v_mfma_f32_16x16x32_bf16 v[2:5], v[110:113], v[114:117], v[2:5]
	v_add_u32_e32 v98, s18, v125
	s_waitcnt vmcnt(6)
	v_cvt_pk_bf16_f32 v34, v34, v35
	v_cvt_pk_bf16_f32 v35, v36, v37
	v_cvt_pk_bf16_f32 v36, v30, v31
	v_add_u32_e32 v30, s19, v126
	v_cvt_pk_bf16_f32 v37, v32, v33
	ds_write_b128 v98, v[34:37]
	s_waitcnt vmcnt(5)
	ds_write_b128 v30, v[26:29]
	v_add_u32_e32 v26, s19, v127
	s_waitcnt vmcnt(4)
	ds_write_b128 v26, v[22:25]
	ds_read_b128 v[22:25], v129 offset:0x400
	ds_read_b128 v[26:29], v129 offset:0xc00
	ds_read_b128 v[30:33], v129 offset:0x1400
	ds_read_b128 v[34:37], v129 offset:0x1c00
	ds_read_b128 v[98:101], v128 offset:0x400
	ds_read_b128 v[102:105], v128 offset:0xc00
	ds_read_b128 v[106:109], v128 offset:0x1400
	s_nop 0
	s_waitcnt lgkmcnt(2)
	s_nop 0
	v_mfma_f32_16x16x32_bf16 v[94:97], v[22:25], v[98:101], v[94:97]
	v_mfma_f32_16x16x32_bf16 v[90:93], v[26:29], v[98:101], v[90:93]
	v_mfma_f32_16x16x32_bf16 v[86:89], v[30:33], v[98:101], v[86:89]
	v_mfma_f32_16x16x32_bf16 v[82:85], v[34:37], v[98:101], v[82:85]
	ds_read_b128 v[98:101], v128 offset:0x1c00
	s_waitcnt lgkmcnt(2)
	s_nop 0
	v_mfma_f32_16x16x32_bf16 v[78:81], v[22:25], v[102:105], v[78:81]
	v_mfma_f32_16x16x32_bf16 v[74:77], v[26:29], v[102:105], v[74:77]
	v_mfma_f32_16x16x32_bf16 v[70:73], v[30:33], v[102:105], v[70:73]
	v_mfma_f32_16x16x32_bf16 v[66:69], v[34:37], v[102:105], v[66:69]
	s_waitcnt lgkmcnt(1)
	s_nop 0
	v_mfma_f32_16x16x32_bf16 v[62:65], v[22:25], v[106:109], v[62:65]
	v_mfma_f32_16x16x32_bf16 v[58:61], v[26:29], v[106:109], v[58:61]
	v_mfma_f32_16x16x32_bf16 v[54:57], v[30:33], v[106:109], v[54:57]
	v_mfma_f32_16x16x32_bf16 v[50:53], v[34:37], v[106:109], v[50:53]
	s_waitcnt lgkmcnt(0)
	s_nop 0
	v_mfma_f32_16x16x32_bf16 v[22:25], v[22:25], v[98:101], v[46:49]
	v_mfma_f32_16x16x32_bf16 v[26:29], v[26:29], v[98:101], v[42:45]
	v_mfma_f32_16x16x32_bf16 v[30:33], v[30:33], v[98:101], v[38:41]
	v_mfma_f32_16x16x32_bf16 v[2:5], v[34:37], v[98:101], v[2:5]
	v_add_u32_e32 v34, s18, v122
	s_waitcnt vmcnt(2)
	v_cvt_pk_bf16_f32 v10, v10, v11
	v_cvt_pk_bf16_f32 v11, v12, v13
	v_cvt_pk_bf16_f32 v12, v6, v7
	v_add_u32_e32 v6, s19, v123
	s_lshl_b64 s[0:1], s[4:5], 1
	v_cvt_pk_bf16_f32 v13, v8, v9
	ds_write_b128 v34, v[10:13]
	s_waitcnt vmcnt(1)
	ds_write_b128 v6, v[18:21]
	v_add_u32_e32 v6, s19, v124
	s_add_u32 s0, s10, s0
	s_waitcnt vmcnt(0)
	ds_write_b128 v6, v[14:17]
	s_addc_u32 s1, s11, s1
	s_lshl_b32 s2, s16, 9
	s_waitcnt lgkmcnt(0)
	s_barrier
	v_add_u32_e32 v110, 0x10000, v128
	v_add_u32_e32 v102, 0x10000, v129
	ds_read_b128 v[6:9], v102 offset:0
	ds_read_b128 v[10:13], v102 offset:0x800
	ds_read_b128 v[14:17], v102 offset:0x1000
	ds_read_b128 v[18:21], v102 offset:0x1800
	ds_read_b128 v[34:37], v110 offset:0
	ds_read_b128 v[38:41], v110 offset:0x800
	ds_read_b128 v[42:45], v110 offset:0x1000
	s_add_u32 s0, s0, s2
	s_addc_u32 s1, s1, 0
	s_lshl_b32 s2, s16, 10
	s_waitcnt lgkmcnt(2)
	s_add_u32 s2, s8, s2
	v_mfma_f32_16x16x32_bf16 v[46:49], v[6:9], v[34:37], v[94:97]
	s_addc_u32 s3, s9, 0
	v_mfma_f32_16x16x32_bf16 v[90:93], v[10:13], v[34:37], v[90:93]
	v_mfma_f32_16x16x32_bf16 v[86:89], v[14:17], v[34:37], v[86:89]
	v_mfma_f32_16x16x32_bf16 v[34:37], v[18:21], v[34:37], v[82:85]
	ds_read_b128 v[82:85], v110 offset:0x1800
	s_waitcnt lgkmcnt(2)
	s_nop 0
	v_mfma_f32_16x16x32_bf16 v[78:81], v[6:9], v[38:41], v[78:81]
	v_mfma_f32_16x16x32_bf16 v[74:77], v[10:13], v[38:41], v[74:77]
	v_mfma_f32_16x16x32_bf16 v[70:73], v[14:17], v[38:41], v[70:73]
	v_mfma_f32_16x16x32_bf16 v[38:41], v[18:21], v[38:41], v[66:69]
	s_waitcnt lgkmcnt(1)
	s_nop 0
	v_mfma_f32_16x16x32_bf16 v[62:65], v[6:9], v[42:45], v[62:65]
	v_mfma_f32_16x16x32_bf16 v[58:61], v[10:13], v[42:45], v[58:61]
	v_mfma_f32_16x16x32_bf16 v[54:57], v[14:17], v[42:45], v[54:57]
	v_mfma_f32_16x16x32_bf16 v[42:45], v[18:21], v[42:45], v[50:53]
	s_waitcnt lgkmcnt(0)
	s_nop 0
	v_mfma_f32_16x16x32_bf16 v[50:53], v[6:9], v[82:85], v[22:25]
	v_mfma_f32_16x16x32_bf16 v[66:69], v[10:13], v[82:85], v[26:29]
	v_mfma_f32_16x16x32_bf16 v[94:97], v[14:17], v[82:85], v[30:33]
	v_mfma_f32_16x16x32_bf16 v[2:5], v[18:21], v[82:85], v[2:5]
	ds_read_b128 v[18:21], v102 offset:0x400
	ds_read_b128 v[82:85], v102 offset:0xc00
	ds_read_b128 v[98:101], v102 offset:0x1400
	ds_read_b128 v[102:105], v102 offset:0x1c00
	ds_read_b128 v[6:9], v110 offset:0x400
	ds_read_b128 v[10:13], v110 offset:0xc00
	ds_read_b128 v[106:109], v110 offset:0x1400
	s_nop 0
	s_waitcnt lgkmcnt(2)
	s_nop 0
	v_mfma_f32_16x16x32_bf16 v[46:49], v[18:21], v[6:9], v[46:49]
	v_mfma_f32_16x16x32_bf16 v[90:93], v[82:85], v[6:9], v[90:93]
	v_mfma_f32_16x16x32_bf16 v[30:33], v[98:101], v[6:9], v[86:89]
	v_mfma_f32_16x16x32_bf16 v[14:17], v[102:105], v[6:9], v[34:37]
	ds_read_b128 v[86:89], v110 offset:0x1c00
	s_waitcnt lgkmcnt(2)
	s_nop 0
	v_mfma_f32_16x16x32_bf16 v[78:81], v[18:21], v[10:13], v[78:81]
	v_mfma_f32_16x16x32_bf16 v[74:77], v[82:85], v[10:13], v[74:77]
	v_mfma_f32_16x16x32_bf16 v[26:29], v[98:101], v[10:13], v[70:73]
	v_mfma_f32_16x16x32_bf16 v[10:13], v[102:105], v[10:13], v[38:41]
	s_waitcnt lgkmcnt(1)
	s_nop 0
	v_mfma_f32_16x16x32_bf16 v[62:65], v[18:21], v[106:109], v[62:65]
	v_mfma_f32_16x16x32_bf16 v[38:41], v[82:85], v[106:109], v[58:61]
	v_mfma_f32_16x16x32_bf16 v[22:25], v[98:101], v[106:109], v[54:57]
	v_mfma_f32_16x16x32_bf16 v[6:9], v[102:105], v[106:109], v[42:45]
	s_waitcnt lgkmcnt(0)
	s_nop 0
	v_mfma_f32_16x16x32_bf16 v[42:45], v[18:21], v[86:89], v[50:53]
	v_mfma_f32_16x16x32_bf16 v[34:37], v[82:85], v[86:89], v[66:69]
	v_mfma_f32_16x16x32_bf16 v[18:21], v[98:101], v[86:89], v[94:97]
	v_mfma_f32_16x16x32_bf16 v[2:5], v[102:105], v[86:89], v[2:5]
	v_lshrrev_b32_e32 v50, 2, v119
	v_and_b32_e32 v50, 12, v50
	v_lshl_or_b32 v66, v121, 6, v50
	v_lshlrev_b32_e32 v67, 2, v66
	s_waitcnt lgkmcnt(0)
	s_barrier
	global_load_dwordx4 v[50:53], v67, s[2:3]
	global_load_dwordx4 v[54:57], v67, s[2:3] offset:64
	v_lshrrev_b32_e32 v58, 1, v119
	v_lshl_or_b32 v59, v120, 6, v118
	v_and_b32_e32 v68, 8, v58
	v_lshl_add_u32 v69, v59, 9, 0
	v_or_b32_e32 v70, 16, v59
	v_or_b32_e32 v71, 48, v59
	v_lshrrev_b32_e32 v58, 3, v66
	v_or_b32_e32 v59, 16, v66
	v_bitop3_b32 v83, v70, v58, 31 bitop3:0x6c
	v_lshrrev_b32_e32 v85, 3, v59
	v_lshl_add_u32 v72, v70, 9, 0
	v_xor_b32_e32 v82, v58, v118
	v_bitop3_b32 v84, v71, v58, 31 bitop3:0x6c
	v_lshlrev_b32_e32 v83, 4, v83
	v_xor_b32_e32 v86, v85, v118
	v_lshl_add_u32 v73, v71, 9, 0
	v_lshlrev_b32_e32 v82, 4, v82
	v_lshlrev_b32_e32 v84, 4, v84
	v_add3_u32 v83, v72, v83, v68
	v_lshlrev_b32_e32 v86, 4, v86
	global_load_dwordx4 v[58:61], v67, s[2:3] offset:128
	v_add3_u32 v82, v69, v82, v68
	v_add3_u32 v84, v73, v84, v68
	v_add3_u32 v86, v69, v86, v68
	s_waitcnt vmcnt(2)
	v_add_f32_e32 v46, v46, v50
	v_add_f32_e32 v47, v47, v51
	v_add_f32_e32 v48, v48, v52
	v_add_f32_e32 v49, v49, v53
	v_add_f32_e32 v78, v78, v50
	v_add_f32_e32 v79, v79, v51
	v_add_f32_e32 v80, v80, v52
	v_add_f32_e32 v81, v81, v53
	v_add_f32_e32 v62, v62, v50
	v_add_f32_e32 v63, v63, v51
	v_add_f32_e32 v42, v42, v50
	v_add_f32_e32 v43, v43, v51
	v_add_f32_e32 v44, v44, v52
	v_add_f32_e32 v45, v45, v53
	s_waitcnt vmcnt(1)
	v_add_f32_e32 v50, v90, v54
	v_add_f32_e32 v51, v91, v55
	v_add_f32_e32 v64, v64, v52
	v_add_f32_e32 v65, v65, v53
	v_add_f32_e32 v52, v92, v56
	v_add_f32_e32 v53, v93, v57
	v_max_f32_e32 v46, 0, v46
	v_max_f32_e32 v47, 0, v47
	v_max_f32_e32 v48, 0, v48
	v_max_f32_e32 v49, 0, v49
	v_max_f32_e32 v78, 0, v78
	v_max_f32_e32 v79, 0, v79
	v_max_f32_e32 v80, 0, v80
	v_max_f32_e32 v81, 0, v81
	v_max_f32_e32 v88, 0, v43
	v_max_f32_e32 v89, 0, v44
	v_max_f32_e32 v90, 0, v45
	v_max_f32_e32 v50, 0, v50
	v_max_f32_e32 v51, 0, v51
	v_cvt_pk_bf16_f32 v43, v48, v49
	v_cvt_pk_bf16_f32 v44, v78, v79
	v_cvt_pk_bf16_f32 v45, v80, v81
	v_max_f32_e32 v62, 0, v62
	v_max_f32_e32 v63, 0, v63
	v_max_f32_e32 v64, 0, v64
	v_max_f32_e32 v65, 0, v65
	v_max_f32_e32 v87, 0, v42
	v_max_f32_e32 v52, 0, v52
	v_max_f32_e32 v53, 0, v53
	v_cvt_pk_bf16_f32 v42, v46, v47
	v_cvt_pk_bf16_f32 v46, v62, v63
	v_cvt_pk_bf16_f32 v47, v64, v65
	v_cvt_pk_bf16_f32 v48, v87, v88
	v_cvt_pk_bf16_f32 v49, v89, v90
	v_cvt_pk_bf16_f32 v50, v50, v51
	v_cvt_pk_bf16_f32 v51, v52, v53
	ds_write_b64 v83, v[44:45]
	ds_write2st64_b64 v82, v[42:43], v[46:47] offset1:32
	ds_write_b64 v84, v[48:49]
	ds_write_b64 v86, v[50:51]
	v_add_f32_e32 v43, v76, v56
	v_add_f32_e32 v44, v77, v57
	v_max_f32_e32 v43, 0, v43
	v_max_f32_e32 v44, 0, v44
	v_add_f32_e32 v42, v75, v55
	v_cvt_pk_bf16_f32 v43, v43, v44
	v_bitop3_b32 v44, v85, v70, 31 bitop3:0x78
	v_add_f32_e32 v74, v74, v54
	v_max_f32_e32 v42, 0, v42
	v_lshlrev_b32_e32 v44, 4, v44
	v_max_f32_e32 v74, 0, v74
	v_cvt_pk_bf16_f32 v42, v74, v42
	v_add3_u32 v44, v72, v44, v68
	ds_write_b64 v44, v[42:43]
	global_load_dwordx4 v[42:45], v67, s[2:3] offset:192
	v_add_f32_e32 v34, v34, v54
	v_add_f32_e32 v35, v35, v55
	v_add_f32_e32 v36, v36, v56
	v_max_f32_e32 v34, 0, v34
	v_max_f32_e32 v35, 0, v35
	v_max_f32_e32 v36, 0, v36
	v_add_f32_e32 v37, v37, v57
	v_max_f32_e32 v37, 0, v37
	v_cvt_pk_bf16_f32 v34, v34, v35
	v_cvt_pk_bf16_f32 v35, v36, v37
	v_bitop3_b32 v36, v85, v71, 31 bitop3:0x78
	v_add_f32_e32 v38, v38, v54
	v_add_f32_e32 v39, v39, v55
	v_lshlrev_b32_e32 v36, 4, v36
	v_max_f32_e32 v38, 0, v38
	v_max_f32_e32 v39, 0, v39
	v_add_f32_e32 v40, v40, v56
	v_add_f32_e32 v41, v41, v57
	v_add3_u32 v36, v73, v36, v68
	v_max_f32_e32 v40, 0, v40
	v_max_f32_e32 v41, 0, v41
	v_cvt_pk_bf16_f32 v38, v38, v39
	v_cvt_pk_bf16_f32 v39, v40, v41
	ds_write_b64 v86, v[38:39] offset:16384
	ds_write_b64 v36, v[34:35]
	v_or_b32_e32 v34, 32, v66
	s_waitcnt vmcnt(1)
	v_add_f32_e32 v30, v30, v58
	v_add_f32_e32 v31, v31, v59
	v_add_f32_e32 v32, v32, v60
	v_add_f32_e32 v26, v26, v58
	v_add_f32_e32 v27, v27, v59
	v_add_f32_e32 v28, v28, v60
	v_add_f32_e32 v18, v18, v58
	v_add_f32_e32 v19, v19, v59
	v_add_f32_e32 v20, v20, v60
	v_lshrrev_b32_e32 v34, 3, v34
	v_max_f32_e32 v30, 0, v30
	v_max_f32_e32 v31, 0, v31
	v_max_f32_e32 v32, 0, v32
	v_add_f32_e32 v33, v33, v61
	v_max_f32_e32 v26, 0, v26
	v_max_f32_e32 v27, 0, v27
	v_max_f32_e32 v28, 0, v28
	v_add_f32_e32 v29, v29, v61
	v_max_f32_e32 v18, 0, v18
	v_max_f32_e32 v19, 0, v19
	v_max_f32_e32 v20, 0, v20
	v_add_f32_e32 v21, v21, v61
	v_max_f32_e32 v33, 0, v33
	v_cvt_pk_bf16_f32 v30, v30, v31
	v_cvt_pk_bf16_f32 v31, v32, v33
	v_xor_b32_e32 v32, v34, v118
	v_max_f32_e32 v29, 0, v29
	v_cvt_pk_bf16_f32 v26, v26, v27
	v_cvt_pk_bf16_f32 v27, v28, v29
	v_bitop3_b32 v28, v34, v70, 31 bitop3:0x78
	v_max_f32_e32 v21, 0, v21
	v_cvt_pk_bf16_f32 v18, v18, v19
	v_cvt_pk_bf16_f32 v19, v20, v21
	v_bitop3_b32 v20, v34, v71, 31 bitop3:0x78
	v_lshlrev_b32_e32 v32, 4, v32
	v_lshlrev_b32_e32 v28, 4, v28
	v_add_f32_e32 v22, v22, v58
	v_add_f32_e32 v23, v23, v59
	v_lshlrev_b32_e32 v20, 4, v20
	v_add3_u32 v32, v69, v32, v68
	v_add3_u32 v28, v72, v28, v68
	v_max_f32_e32 v22, 0, v22
	v_max_f32_e32 v23, 0, v23
	v_add_f32_e32 v24, v24, v60
	v_add_f32_e32 v25, v25, v61
	v_add3_u32 v20, v73, v20, v68
	ds_write_b64 v32, v[30:31]
	ds_write_b64 v28, v[26:27]
	v_max_f32_e32 v24, 0, v24
	v_max_f32_e32 v25, 0, v25
	v_cvt_pk_bf16_f32 v22, v22, v23
	v_cvt_pk_bf16_f32 v23, v24, v25
	ds_write_b64 v32, v[22:23] offset:16384
	ds_write_b64 v20, v[18:19]
	v_or_b32_e32 v18, 48, v66
	s_waitcnt vmcnt(0)
	v_add_f32_e32 v14, v14, v42
	v_add_f32_e32 v15, v15, v43
	v_add_f32_e32 v16, v16, v44
	v_add_f32_e32 v10, v10, v42
	v_add_f32_e32 v11, v11, v43
	v_add_f32_e32 v12, v12, v44
	v_add_f32_e32 v2, v2, v42
	v_add_f32_e32 v3, v3, v43
	v_add_f32_e32 v4, v4, v44
	v_lshrrev_b32_e32 v18, 3, v18
	v_max_f32_e32 v14, 0, v14
	v_max_f32_e32 v15, 0, v15
	v_max_f32_e32 v16, 0, v16
	v_add_f32_e32 v17, v17, v45
	v_max_f32_e32 v10, 0, v10
	v_max_f32_e32 v11, 0, v11
	v_max_f32_e32 v12, 0, v12
	v_add_f32_e32 v13, v13, v45
	v_max_f32_e32 v2, 0, v2
	v_max_f32_e32 v3, 0, v3
	v_max_f32_e32 v4, 0, v4
	v_add_f32_e32 v5, v5, v45
	v_max_f32_e32 v17, 0, v17
	v_cvt_pk_bf16_f32 v14, v14, v15
	v_cvt_pk_bf16_f32 v15, v16, v17
	v_xor_b32_e32 v16, v18, v118
	v_max_f32_e32 v13, 0, v13
	v_cvt_pk_bf16_f32 v10, v10, v11
	v_cvt_pk_bf16_f32 v11, v12, v13
	v_bitop3_b32 v12, v18, v70, 31 bitop3:0x78
	v_max_f32_e32 v5, 0, v5
	v_cvt_pk_bf16_f32 v2, v2, v3
	v_cvt_pk_bf16_f32 v3, v4, v5
	v_bitop3_b32 v4, v18, v71, 31 bitop3:0x78
	v_lshlrev_b32_e32 v16, 4, v16
	v_lshlrev_b32_e32 v12, 4, v12
	v_add_f32_e32 v6, v6, v42
	v_add_f32_e32 v7, v7, v43
	v_lshlrev_b32_e32 v4, 4, v4
	v_add3_u32 v16, v69, v16, v68
	v_add3_u32 v12, v72, v12, v68
	v_max_f32_e32 v6, 0, v6
	v_max_f32_e32 v7, 0, v7
	v_add_f32_e32 v8, v8, v44
	v_add_f32_e32 v9, v9, v45
	v_add3_u32 v4, v73, v4, v68
	ds_write_b64 v16, v[14:15]
	ds_write_b64 v12, v[10:11]
	v_max_f32_e32 v8, 0, v8
	v_max_f32_e32 v9, 0, v9
	v_cvt_pk_bf16_f32 v6, v6, v7
	v_cvt_pk_bf16_f32 v7, v8, v9
	ds_write_b64 v16, v[6:7] offset:16384
	ds_write_b64 v4, v[2:3]
	v_and_b32_e32 v2, 0x1f0, v1
	v_mov_b32_e32 v3, 0
	v_lshl_add_u64 v[2:3], s[0:1], 0, v[2:3]
	s_mov_b64 s[0:1], 0x2000000
	v_ashrrev_i32_e32 v6, 5, v0
	v_lshl_add_u64 v[10:11], v[2:3], 0, s[0:1]
	v_xor_b32_e32 v2, v6, v0
	v_lshlrev_b32_e32 v2, 4, v2
	v_lshlrev_b32_e32 v1, 9, v6
	v_and_b32_e32 v2, 0x1f0, v2
	v_add3_u32 v1, 0, v1, v2
	s_waitcnt lgkmcnt(0)
	s_barrier
	ds_read_b128 v[2:5], v1
	v_ashrrev_i32_e32 v7, 31, v6
	v_add_u32_e32 v1, 0x200, v0
	v_lshlrev_b64 v[6:7], 11, v[6:7]
	v_ashrrev_i32_e32 v14, 5, v1
	v_lshl_add_u64 v[12:13], v[10:11], 0, v[6:7]
	v_xor_b32_e32 v6, v14, v0
	v_lshlrev_b32_e32 v6, 4, v6
	v_lshlrev_b32_e32 v1, 9, v14
	v_and_b32_e32 v6, 0x1f0, v6
	v_add3_u32 v1, 0, v1, v6
	ds_read_b128 v[6:9], v1
	v_ashrrev_i32_e32 v15, 31, v14
	s_waitcnt lgkmcnt(1)
	global_store_dwordx4 v[12:13], v[2:5], off sc1
	v_add_u32_e32 v1, 0x400, v0
	s_nop 0
	v_lshlrev_b64 v[2:3], 11, v[14:15]
	v_lshl_add_u64 v[2:3], v[10:11], 0, v[2:3]
	s_waitcnt lgkmcnt(0)
	global_store_dwordx4 v[2:3], v[6:9], off sc1
	s_nop 1
	v_ashrrev_i32_e32 v6, 5, v1
	v_xor_b32_e32 v2, v6, v0
	v_lshlrev_b32_e32 v2, 4, v2
	v_lshlrev_b32_e32 v1, 9, v6
	v_and_b32_e32 v2, 0x1f0, v2
	v_add3_u32 v1, 0, v1, v2
	ds_read_b128 v[2:5], v1
	v_ashrrev_i32_e32 v7, 31, v6
	v_add_u32_e32 v1, 0x600, v0
	v_lshlrev_b64 v[6:7], 11, v[6:7]
	v_ashrrev_i32_e32 v14, 5, v1
	v_lshl_add_u64 v[12:13], v[10:11], 0, v[6:7]
	v_xor_b32_e32 v6, v14, v0
	v_lshlrev_b32_e32 v6, 4, v6
	v_lshlrev_b32_e32 v1, 9, v14
	v_and_b32_e32 v6, 0x1f0, v6
	v_add3_u32 v1, 0, v1, v6
	ds_read_b128 v[6:9], v1
	v_ashrrev_i32_e32 v15, 31, v14
	s_waitcnt lgkmcnt(1)
	global_store_dwordx4 v[12:13], v[2:5], off sc1
	v_add_u32_e32 v1, 0x800, v0
	s_nop 0
	v_lshlrev_b64 v[2:3], 11, v[14:15]
	v_lshl_add_u64 v[2:3], v[10:11], 0, v[2:3]
	s_waitcnt lgkmcnt(0)
	global_store_dwordx4 v[2:3], v[6:9], off sc1
	s_nop 1
	v_ashrrev_i32_e32 v6, 5, v1
	v_xor_b32_e32 v2, v6, v0
	v_lshlrev_b32_e32 v2, 4, v2
	v_lshlrev_b32_e32 v1, 9, v6
	v_and_b32_e32 v2, 0x1f0, v2
	v_add3_u32 v1, 0, v1, v2
	ds_read_b128 v[2:5], v1
	v_ashrrev_i32_e32 v7, 31, v6
	v_add_u32_e32 v1, 0xa00, v0
	v_lshlrev_b64 v[6:7], 11, v[6:7]
	v_ashrrev_i32_e32 v14, 5, v1
	v_lshl_add_u64 v[12:13], v[10:11], 0, v[6:7]
	v_xor_b32_e32 v6, v14, v0
	v_lshlrev_b32_e32 v6, 4, v6
	v_lshlrev_b32_e32 v1, 9, v14
	v_and_b32_e32 v6, 0x1f0, v6
	v_add3_u32 v1, 0, v1, v6
	ds_read_b128 v[6:9], v1
	v_ashrrev_i32_e32 v15, 31, v14
	s_waitcnt lgkmcnt(1)
	global_store_dwordx4 v[12:13], v[2:5], off sc1
	v_add_u32_e32 v1, 0xc00, v0
	s_nop 0
	v_lshlrev_b64 v[2:3], 11, v[14:15]
	v_lshl_add_u64 v[2:3], v[10:11], 0, v[2:3]
	s_waitcnt lgkmcnt(0)
	global_store_dwordx4 v[2:3], v[6:9], off sc1
	s_nop 1
	v_ashrrev_i32_e32 v6, 5, v1
	v_xor_b32_e32 v2, v6, v0
	v_lshlrev_b32_e32 v2, 4, v2
	v_lshlrev_b32_e32 v1, 9, v6
	v_and_b32_e32 v2, 0x1f0, v2
	v_add3_u32 v1, 0, v1, v2
	ds_read_b128 v[2:5], v1
	v_add_u32_e32 v1, 0xe00, v0
	v_ashrrev_i32_e32 v14, 5, v1
	v_xor_b32_e32 v0, v14, v0
	v_lshlrev_b32_e32 v0, 4, v0
	v_ashrrev_i32_e32 v7, 31, v6
	v_lshlrev_b32_e32 v1, 9, v14
	v_and_b32_e32 v0, 0x1f0, v0
	v_lshlrev_b64 v[6:7], 11, v[6:7]
	v_add3_u32 v0, 0, v1, v0
	v_lshl_add_u64 v[12:13], v[10:11], 0, v[6:7]
	ds_read_b128 v[6:9], v0
	v_ashrrev_i32_e32 v15, 31, v14
	v_lshlrev_b64 v[0:1], 11, v[14:15]
	v_lshl_add_u64 v[0:1], v[10:11], 0, v[0:1]
	s_waitcnt lgkmcnt(1)
	global_store_dwordx4 v[12:13], v[2:5], off sc1
	s_waitcnt lgkmcnt(0)
	global_store_dwordx4 v[0:1], v[6:9], off sc1
	s_endpgm
